# GEMM K-loops: vmcnt and lgkmcnt waits ahead of each barrier merged into one s_waitcnt
# speedup vs baseline: 1.0195x; 1.0019x over previous
; #define PG8_STAGE(bufoff, gbase, voff) do { _Pragma("unroll") for (int _i = 0; _i < 2; ++_i) \
;         __builtin_amdgcn_global_load_lds((const unsigned*)((const char*)(gbase) + (voff)[_i]), (PG8_LAS unsigned*)(lds + (bufoff) + ldsw + _i * 8192), 16, 0, 0); } while (0)
; #define PG8_LDA(dst, b, h) do { _Pragma("unroll") for (int m = 0; m < 4; ++m) _Pragma("unroll") for (int k = 0; k < 2; ++k) dst[m][k] = *(const PG8_LAS bf16x8*)(lds + PG8_SA(b, h) + aoff + m * 2048 + k * 1024); } while (0)
; #define PG8_LDB(dst, b, h) do { _Pragma("unroll") for (int n = 0; n < 2; ++n) _Pragma("unroll") for (int k = 0; k < 2; ++k) dst[n][k] = *(const PG8_LAS bf16x8*)(lds + PG8_SB(b, h) + boff + n * 2048 + k * 1024); } while (0)
; #define PG8_MMA(ai, bj, At, Bt) do { __builtin_amdgcn_s_setprio(1); _Pragma("unroll") for (int m = 0; m < 4; ++m) _Pragma("unroll") for (int n = 0; n < 2; ++n) _Pragma("unroll") for (int k = 0; k < 2; ++k) \
;         acc[ai][bj][m][n] = __builtin_amdgcn_mfma_f32_16x16x32_bf16(Bt[n][k], At[m][k], acc[ai][bj][m][n], 0, 0, 0); __builtin_amdgcn_s_setprio(0); } while (0)
; #define PG8_WAIT_V(n) asm volatile("s_waitcnt vmcnt(" #n ")" ::: "memory")
; #define PG8_WAIT_L(n) asm volatile("s_waitcnt lgkmcnt(" #n ")" ::: "memory")
; template <class Epi, class Sched, bool ALIGN_EPI = false, bool SP2 = false>
; __device__ __forceinline__ void gemm_phase(PG8_LAS unsigned char* lds, const Gemm g, const Sched& S, const Epi& E) {
;     ...
;             const bool last = (t == nt - 2);
;             const char* a1 = cA + (size_t)(t + 1) * kstep;
;             const char* a2 = last ? nA : cA + (size_t)(t + 2) * kstep; const char* b2 = last ? nB : cB + (size_t)(t + 2) * kstep;
;             const char* a3 = a2 + kstep; const char* b3 = b2 + kstep;
;             if (last && has_next) S.a_ready(nxt);
;             if constexpr (SP2) {
;             PG8_LDB(B0, 0, 0); PG8_LDB(B1, 0, 1); PG8_SCHED; PG8_LDA(At, 0, 0); PG8_STAGEA(PG8_SA(1, 1), a1, 1, false);
;             PG8_WAIT_V(8); PG8_WAIT_L(0); PG8_BAR; PG8_MMA(0, 0, At, B0); PG8_MMA(0, 1, At, B1); PG8_BAR; PG8_SCHED;
;             PG8_LDA(At, 0, 1); PG8_STAGE(PG8_SB(0, 0), b2, voffB); PG8_STAGE(PG8_SB(0, 1), b2 + hstep, voffB); PG8_STAGEA(PG8_SA(0, 0), a2, 0, last);
;             PG8_WAIT_V(8); PG8_WAIT_L(0); PG8_BAR; PG8_MMA(1, 0, At, B0); PG8_MMA(1, 1, At, B1); PG8_BAR; PG8_SCHED;
.LBB0_110:
	v_add_u32_e32 v142, s79, v170
	v_add_u32_e32 v175, s80, v170
	ds_read_b128 v[130:133], v142
	ds_read_b128 v[134:137], v142 offset:1024
	ds_read_b128 v[138:141], v142 offset:2048
	ds_read_b128 v[142:145], v142 offset:3072
	ds_read_b128 v[162:165], v175
	ds_read_b128 v[166:169], v175 offset:1024
	ds_read_b128 v[176:179], v175 offset:2048
	ds_read_b128 v[180:183], v175 offset:3072
	s_add_u32 s54, s10, 0xfff80080
	s_addc_u32 s55, s11, -1
	s_cmp_eq_u32 s49, 28
	s_cselect_b32 s61, s9, s55
	s_cselect_b32 s60, s18, s54
	s_cselect_b32 s55, s19, s47
	s_cselect_b32 s54, s36, s37
	v_lshl_add_u64 v[200:201], s[10:11], 0, v[154:155]
	s_add_i32 m0, s57, 0xc000
	ds_read_b128 v[184:187], v174
	ds_read_b128 v[188:191], v174 offset:1024
	ds_read_b128 v[192:195], v174 offset:2048
	ds_read_b128 v[196:199], v174 offset:3072
	ds_read_b128 v[204:207], v174 offset:4096
	ds_read_b128 v[208:211], v174 offset:5120
	ds_read_b128 v[212:215], v174 offset:6144
	ds_read_b128 v[216:219], v174 offset:7168
	global_load_lds_dwordx4 v[200:201], off
	v_lshl_add_u64 v[200:201], s[10:11], 0, v[156:157]
	s_add_i32 m0, s57, 0xe000
	s_nop 0
	global_load_lds_dwordx4 v[200:201], off
	s_waitcnt vmcnt(8) lgkmcnt(0)
	s_barrier
	s_setprio 1
	v_mfma_f32_16x16x32_bf16 v[114:117], v[130:133], v[184:187], v[114:117]
	v_mfma_f32_16x16x32_bf16 v[118:121], v[138:141], v[184:187], v[118:121]
	v_mfma_f32_16x16x32_bf16 v[98:101], v[130:133], v[192:195], v[98:101]
	v_mfma_f32_16x16x32_bf16 v[102:105], v[138:141], v[192:195], v[102:105]
	v_mfma_f32_16x16x32_bf16 v[82:85], v[130:133], v[204:207], v[82:85]
	v_mfma_f32_16x16x32_bf16 v[86:89], v[138:141], v[204:207], v[86:89]
	v_mfma_f32_16x16x32_bf16 v[66:69], v[130:133], v[212:215], v[66:69]
	v_mfma_f32_16x16x32_bf16 v[70:73], v[138:141], v[212:215], v[70:73]
	v_mfma_f32_16x16x32_bf16 v[114:117], v[134:137], v[188:191], v[114:117]
	v_mfma_f32_16x16x32_bf16 v[118:121], v[142:145], v[188:191], v[118:121]
	v_mfma_f32_16x16x32_bf16 v[98:101], v[134:137], v[196:199], v[98:101]
	v_mfma_f32_16x16x32_bf16 v[102:105], v[142:145], v[196:199], v[102:105]
	v_mfma_f32_16x16x32_bf16 v[82:85], v[134:137], v[208:211], v[82:85]
	v_mfma_f32_16x16x32_bf16 v[86:89], v[142:145], v[208:211], v[86:89]
	v_mfma_f32_16x16x32_bf16 v[66:69], v[134:137], v[216:219], v[66:69]
	v_mfma_f32_16x16x32_bf16 v[70:73], v[142:145], v[216:219], v[70:73]
	v_mfma_f32_16x16x32_bf16 v[122:125], v[162:165], v[184:187], v[122:125]
	v_mfma_f32_16x16x32_bf16 v[126:129], v[176:179], v[184:187], v[126:129]
	v_mfma_f32_16x16x32_bf16 v[106:109], v[162:165], v[192:195], v[106:109]
	v_mfma_f32_16x16x32_bf16 v[110:113], v[176:179], v[192:195], v[110:113]
	v_mfma_f32_16x16x32_bf16 v[90:93], v[162:165], v[204:207], v[90:93]
	v_mfma_f32_16x16x32_bf16 v[94:97], v[176:179], v[204:207], v[94:97]
	v_mfma_f32_16x16x32_bf16 v[74:77], v[162:165], v[212:215], v[74:77]
	v_mfma_f32_16x16x32_bf16 v[78:81], v[176:179], v[212:215], v[78:81]
	v_mfma_f32_16x16x32_bf16 v[122:125], v[166:169], v[188:191], v[122:125]
	v_mfma_f32_16x16x32_bf16 v[126:129], v[180:183], v[188:191], v[126:129]
	v_mfma_f32_16x16x32_bf16 v[106:109], v[166:169], v[196:199], v[106:109]
	v_mfma_f32_16x16x32_bf16 v[110:113], v[180:183], v[196:199], v[110:113]
	v_mfma_f32_16x16x32_bf16 v[90:93], v[166:169], v[208:211], v[90:93]
	v_mfma_f32_16x16x32_bf16 v[94:97], v[180:183], v[208:211], v[94:97]
	v_mfma_f32_16x16x32_bf16 v[74:77], v[166:169], v[216:219], v[74:77]
	v_mfma_f32_16x16x32_bf16 v[78:81], v[180:183], v[216:219], v[78:81]
	s_setprio 0
	s_barrier
	s_add_i32 s59, s79, s66
	v_lshl_add_u64 v[200:201], s[54:55], 0, v[148:149]
	s_mov_b32 m0, s59
	ds_read_b128 v[184:187], v174 offset:16384
	ds_read_b128 v[188:191], v174 offset:17408
	ds_read_b128 v[192:195], v174 offset:18432
	ds_read_b128 v[196:199], v174 offset:19456
	ds_read_b128 v[204:207], v174 offset:20480
	ds_read_b128 v[208:211], v174 offset:21504
	ds_read_b128 v[212:215], v174 offset:22528
	ds_read_b128 v[216:219], v174 offset:23552
	global_load_lds_dwordx4 v[200:201], off
	s_add_i32 m0, s59, 0x2000
	s_add_u32 s62, s54, 0x80000
	v_lshl_add_u64 v[220:221], s[54:55], 0, v[152:153]
	s_addc_u32 s63, s55, 0
	s_add_i32 s59, s80, s66
	global_load_lds_dwordx4 v[220:221], off
	v_lshl_add_u64 v[222:223], s[62:63], 0, v[148:149]
	s_mov_b32 m0, s59
	v_lshl_add_u64 v[224:225], s[60:61], 0, v[150:151]
	global_load_lds_dwordx4 v[222:223], off
	v_lshl_add_u64 v[222:223], s[62:63], 0, v[152:153]
	s_add_i32 m0, s59, 0x2000
	s_nop 0
	global_load_lds_dwordx4 v[222:223], off
	v_lshl_add_u64 v[222:223], s[60:61], 0, v[146:147]
	s_mov_b32 m0, s57
	s_nop 0
	global_load_lds_dwordx4 v[222:223], off
	s_mov_b32 m0, s67
	s_nop 0
	global_load_lds_dwordx4 v[224:225], off
	s_waitcnt vmcnt(8) lgkmcnt(0)
	s_barrier
; #define PG8_LDA(dst, b, h) do { _Pragma("unroll") for (int m = 0; m < 4; ++m) _Pragma("unroll") for (int k = 0; k < 2; ++k) dst[m][k] = *(const PG8_LAS bf16x8*)(lds + PG8_SA(b, h) + aoff + m * 2048 + k * 1024); } while (0)
; #define PG8_LDB(dst, b, h) do { _Pragma("unroll") for (int n = 0; n < 2; ++n) _Pragma("unroll") for (int k = 0; k < 2; ++k) dst[n][k] = *(const PG8_LAS bf16x8*)(lds + PG8_SB(b, h) + boff + n * 2048 + k * 1024); } while (0)
; #define PG8_MMA(ai, bj, At, Bt) do { __builtin_amdgcn_s_setprio(1); _Pragma("unroll") for (int m = 0; m < 4; ++m) _Pragma("unroll") for (int n = 0; n < 2; ++n) _Pragma("unroll") for (int k = 0; k < 2; ++k) \
;         acc[ai][bj][m][n] = __builtin_amdgcn_mfma_f32_16x16x32_bf16(Bt[n][k], At[m][k], acc[ai][bj][m][n], 0, 0, 0); __builtin_amdgcn_s_setprio(0); } while (0)
; #define PG8_WAIT_V(n) asm volatile("s_waitcnt vmcnt(" #n ")" ::: "memory")
; #define PG8_WAIT_L(n) asm volatile("s_waitcnt lgkmcnt(" #n ")" ::: "memory")
; #define PG8_BAR __builtin_amdgcn_s_barrier()
; #define PG8_SCHED __builtin_amdgcn_sched_barrier(0)
; template <class Epi, class Sched, bool ALIGN_EPI = false, bool SP2 = false>
; __device__ __forceinline__ void gemm_phase(PG8_LAS unsigned char* lds, const Gemm g, const Sched& S, const Epi& E) {
;     ...
;             PG8_WAIT_V(8); PG8_WAIT_L(0); PG8_BAR; PG8_MMA(1, 0, At, B0); PG8_MMA(1, 1, At, B1); PG8_BAR; PG8_SCHED;
;             PG8_LDB(B0, 1, 0); PG8_LDB(B1, 1, 1); PG8_SCHED; PG8_LDA(At, 1, 0); PG8_STAGEA(PG8_SA(0, 1), a2, 1, last);
;             PG8_WAIT_V(8); PG8_WAIT_L(0); PG8_BAR; PG8_MMA(0, 0, At, B0); PG8_MMA(0, 1, At, B1); PG8_BAR; PG8_SCHED;
	s_setprio 1
	v_mfma_f32_16x16x32_bf16 v[58:61], v[130:133], v[184:187], v[58:61]
	v_mfma_f32_16x16x32_bf16 v[62:65], v[138:141], v[184:187], v[62:65]
	v_mfma_f32_16x16x32_bf16 v[42:45], v[130:133], v[192:195], v[42:45]
	v_mfma_f32_16x16x32_bf16 v[46:49], v[138:141], v[192:195], v[46:49]
	v_mfma_f32_16x16x32_bf16 v[18:21], v[130:133], v[204:207], v[18:21]
	v_mfma_f32_16x16x32_bf16 v[22:25], v[138:141], v[204:207], v[22:25]
	v_mfma_f32_16x16x32_bf16 v[6:9], v[130:133], v[212:215], v[6:9]
	v_mfma_f32_16x16x32_bf16 v[14:17], v[138:141], v[212:215], v[14:17]
	v_mfma_f32_16x16x32_bf16 v[58:61], v[134:137], v[188:191], v[58:61]
	v_mfma_f32_16x16x32_bf16 v[62:65], v[142:145], v[188:191], v[62:65]
	v_mfma_f32_16x16x32_bf16 v[42:45], v[134:137], v[196:199], v[42:45]
	v_mfma_f32_16x16x32_bf16 v[46:49], v[142:145], v[196:199], v[46:49]
	v_mfma_f32_16x16x32_bf16 v[18:21], v[134:137], v[208:211], v[18:21]
	v_mfma_f32_16x16x32_bf16 v[22:25], v[142:145], v[208:211], v[22:25]
	v_mfma_f32_16x16x32_bf16 v[6:9], v[134:137], v[216:219], v[6:9]
	v_mfma_f32_16x16x32_bf16 v[14:17], v[142:145], v[216:219], v[14:17]
	v_mfma_f32_16x16x32_bf16 v[50:53], v[162:165], v[184:187], v[50:53]
	v_mfma_f32_16x16x32_bf16 v[54:57], v[176:179], v[184:187], v[54:57]
	v_mfma_f32_16x16x32_bf16 v[34:37], v[162:165], v[192:195], v[34:37]
	v_mfma_f32_16x16x32_bf16 v[38:41], v[176:179], v[192:195], v[38:41]
	v_mfma_f32_16x16x32_bf16 v[26:29], v[162:165], v[204:207], v[26:29]
	v_mfma_f32_16x16x32_bf16 v[30:33], v[176:179], v[204:207], v[30:33]
	v_mfma_f32_16x16x32_bf16 v[10:13], v[162:165], v[212:215], v[10:13]
	v_mfma_f32_16x16x32_bf16 v[2:5], v[176:179], v[212:215], v[2:5]
	v_mfma_f32_16x16x32_bf16 v[50:53], v[166:169], v[188:191], v[50:53]
	v_mfma_f32_16x16x32_bf16 v[54:57], v[180:183], v[188:191], v[54:57]
	v_mfma_f32_16x16x32_bf16 v[34:37], v[166:169], v[196:199], v[34:37]
	v_mfma_f32_16x16x32_bf16 v[38:41], v[180:183], v[196:199], v[38:41]
	v_mfma_f32_16x16x32_bf16 v[26:29], v[166:169], v[208:211], v[26:29]
	v_mfma_f32_16x16x32_bf16 v[30:33], v[180:183], v[208:211], v[30:33]
	v_mfma_f32_16x16x32_bf16 v[10:13], v[166:169], v[216:219], v[10:13]
	v_mfma_f32_16x16x32_bf16 v[2:5], v[180:183], v[216:219], v[2:5]
	s_setprio 0
	s_barrier
	s_add_i32 s59, 0, 0x18000
	s_add_i32 s62, 0, 0x1c000
	v_add_u32_e32 v142, s59, v170
	v_add_u32_e32 v175, s62, v170
	ds_read_b128 v[130:133], v142
	ds_read_b128 v[134:137], v142 offset:1024
	ds_read_b128 v[138:141], v142 offset:2048
	ds_read_b128 v[142:145], v142 offset:3072
	ds_read_b128 v[162:165], v175
	ds_read_b128 v[166:169], v175 offset:1024
	ds_read_b128 v[176:179], v175 offset:2048
	ds_read_b128 v[180:183], v175 offset:3072
	s_add_u32 s60, s60, 0x80000
	s_addc_u32 s61, s61, 0
	s_mov_b32 m0, s68
	v_lshl_add_u64 v[226:227], s[60:61], 0, v[146:147]
	ds_read_b128 v[184:187], v174 offset:32768
	ds_read_b128 v[188:191], v174 offset:33792
	ds_read_b128 v[192:195], v174 offset:34816
	ds_read_b128 v[196:199], v174 offset:35840
	ds_read_b128 v[204:207], v174 offset:36864
	ds_read_b128 v[208:211], v174 offset:37888
	ds_read_b128 v[212:215], v174 offset:38912
	ds_read_b128 v[216:219], v174 offset:39936
	global_load_lds_dwordx4 v[226:227], off
	v_lshl_add_u64 v[226:227], s[60:61], 0, v[150:151]
	s_mov_b32 m0, s69
	s_nop 0
	global_load_lds_dwordx4 v[226:227], off
	s_waitcnt vmcnt(8) lgkmcnt(0)
	s_barrier
	s_setprio 1
	v_mfma_f32_16x16x32_bf16 v[114:117], v[130:133], v[184:187], v[114:117]
	v_mfma_f32_16x16x32_bf16 v[118:121], v[138:141], v[184:187], v[118:121]
	v_mfma_f32_16x16x32_bf16 v[98:101], v[130:133], v[192:195], v[98:101]
	v_mfma_f32_16x16x32_bf16 v[102:105], v[138:141], v[192:195], v[102:105]
	v_mfma_f32_16x16x32_bf16 v[82:85], v[130:133], v[204:207], v[82:85]
	v_mfma_f32_16x16x32_bf16 v[86:89], v[138:141], v[204:207], v[86:89]
	v_mfma_f32_16x16x32_bf16 v[66:69], v[130:133], v[212:215], v[66:69]
	v_mfma_f32_16x16x32_bf16 v[70:73], v[138:141], v[212:215], v[70:73]
	v_mfma_f32_16x16x32_bf16 v[114:117], v[134:137], v[188:191], v[114:117]
	v_mfma_f32_16x16x32_bf16 v[118:121], v[142:145], v[188:191], v[118:121]
	v_mfma_f32_16x16x32_bf16 v[98:101], v[134:137], v[196:199], v[98:101]
	v_mfma_f32_16x16x32_bf16 v[102:105], v[142:145], v[196:199], v[102:105]
	v_mfma_f32_16x16x32_bf16 v[82:85], v[134:137], v[208:211], v[82:85]
	v_mfma_f32_16x16x32_bf16 v[86:89], v[142:145], v[208:211], v[86:89]
	v_mfma_f32_16x16x32_bf16 v[66:69], v[134:137], v[216:219], v[66:69]
	v_mfma_f32_16x16x32_bf16 v[70:73], v[142:145], v[216:219], v[70:73]
	v_mfma_f32_16x16x32_bf16 v[122:125], v[162:165], v[184:187], v[122:125]
	v_mfma_f32_16x16x32_bf16 v[126:129], v[176:179], v[184:187], v[126:129]
	v_mfma_f32_16x16x32_bf16 v[106:109], v[162:165], v[192:195], v[106:109]
	v_mfma_f32_16x16x32_bf16 v[110:113], v[176:179], v[192:195], v[110:113]
	v_mfma_f32_16x16x32_bf16 v[90:93], v[162:165], v[204:207], v[90:93]
	v_mfma_f32_16x16x32_bf16 v[94:97], v[176:179], v[204:207], v[94:97]
	v_mfma_f32_16x16x32_bf16 v[74:77], v[162:165], v[212:215], v[74:77]
	v_mfma_f32_16x16x32_bf16 v[78:81], v[176:179], v[212:215], v[78:81]
	v_mfma_f32_16x16x32_bf16 v[122:125], v[166:169], v[188:191], v[122:125]
	v_mfma_f32_16x16x32_bf16 v[126:129], v[180:183], v[188:191], v[126:129]
	v_mfma_f32_16x16x32_bf16 v[106:109], v[166:169], v[196:199], v[106:109]
	v_mfma_f32_16x16x32_bf16 v[110:113], v[180:183], v[196:199], v[110:113]
	v_mfma_f32_16x16x32_bf16 v[90:93], v[166:169], v[208:211], v[90:93]
	v_mfma_f32_16x16x32_bf16 v[94:97], v[180:183], v[208:211], v[94:97]
	v_mfma_f32_16x16x32_bf16 v[74:77], v[166:169], v[216:219], v[74:77]
	v_mfma_f32_16x16x32_bf16 v[78:81], v[180:183], v[216:219], v[78:81]
	s_setprio 0
	s_barrier
; #define PG8_STAGE(bufoff, gbase, voff) do { _Pragma("unroll") for (int _i = 0; _i < 2; ++_i) \
;         __builtin_amdgcn_global_load_lds((const unsigned*)((const char*)(gbase) + (voff)[_i]), (PG8_LAS unsigned*)(lds + (bufoff) + ldsw + _i * 8192), 16, 0, 0); } while (0)
; #define PG8_LDA(dst, b, h) do { _Pragma("unroll") for (int m = 0; m < 4; ++m) _Pragma("unroll") for (int k = 0; k < 2; ++k) dst[m][k] = *(const PG8_LAS bf16x8*)(lds + PG8_SA(b, h) + aoff + m * 2048 + k * 1024); } while (0)
; #define PG8_MMA(ai, bj, At, Bt) do { __builtin_amdgcn_s_setprio(1); _Pragma("unroll") for (int m = 0; m < 4; ++m) _Pragma("unroll") for (int n = 0; n < 2; ++n) _Pragma("unroll") for (int k = 0; k < 2; ++k) \
;         acc[ai][bj][m][n] = __builtin_amdgcn_mfma_f32_16x16x32_bf16(Bt[n][k], At[m][k], acc[ai][bj][m][n], 0, 0, 0); __builtin_amdgcn_s_setprio(0); } while (0)
; #define PG8_WAIT_V(n) asm volatile("s_waitcnt vmcnt(" #n ")" ::: "memory")
; #define PG8_WAIT_L(n) asm volatile("s_waitcnt lgkmcnt(" #n ")" ::: "memory")
; #define PG8_BAR __builtin_amdgcn_s_barrier()
; #define PG8_SCHED __builtin_amdgcn_sched_barrier(0)
; template <class Epi, class Sched, bool ALIGN_EPI = false, bool SP2 = false>
; __device__ __forceinline__ void gemm_phase(PG8_LAS unsigned char* lds, const Gemm g, const Sched& S, const Epi& E) {
;     ...
;             PG8_LDA(At, 1, 1); PG8_STAGE(PG8_SB(1, 0), b3, voffB); PG8_STAGE(PG8_SB(1, 1), b3 + hstep, voffB); PG8_STAGEA(PG8_SA(1, 0), a3, 0, last);
;             PG8_WAIT_V(8); PG8_WAIT_L(0); PG8_BAR; PG8_MMA(1, 0, At, B0); PG8_MMA(1, 1, At, B1); PG8_BAR; PG8_SCHED;
	s_add_i32 s59, s59, s66
	v_lshl_add_u64 v[200:201], v[200:201], 0, s[26:27]
	s_mov_b32 m0, s59
	ds_read_b128 v[184:187], v174 offset:49152
	ds_read_b128 v[188:191], v174 offset:50176
	ds_read_b128 v[192:195], v174 offset:51200
	ds_read_b128 v[196:199], v174 offset:52224
	ds_read_b128 v[204:207], v174 offset:53248
	ds_read_b128 v[208:211], v174 offset:54272
	ds_read_b128 v[212:215], v174 offset:55296
	ds_read_b128 v[216:219], v174 offset:56320
	global_load_lds_dwordx4 v[200:201], off
	s_add_i32 m0, s59, 0x2000
	s_add_u32 s54, s54, 0x80080
	v_lshl_add_u64 v[200:201], v[220:221], 0, s[26:27]
	s_addc_u32 s55, s55, 0
	s_add_i32 s59, s62, s66
	global_load_lds_dwordx4 v[200:201], off
	v_lshl_add_u64 v[200:201], s[54:55], 0, v[148:149]
	s_mov_b32 m0, s59
	s_nop 0
	global_load_lds_dwordx4 v[200:201], off
	v_lshl_add_u64 v[200:201], s[54:55], 0, v[152:153]
	s_add_i32 m0, s59, 0x2000
	s_nop 0
	global_load_lds_dwordx4 v[200:201], off
	v_lshl_add_u64 v[200:201], v[222:223], 0, s[26:27]
	s_mov_b32 m0, s74
	s_nop 0
	global_load_lds_dwordx4 v[200:201], off
	v_lshl_add_u64 v[200:201], v[224:225], 0, s[26:27]
	s_mov_b32 m0, s75
	s_nop 0
	global_load_lds_dwordx4 v[200:201], off
	s_waitcnt vmcnt(8) lgkmcnt(0)
	s_barrier
	s_setprio 1
	v_mfma_f32_16x16x32_bf16 v[58:61], v[130:133], v[184:187], v[58:61]
	v_mfma_f32_16x16x32_bf16 v[62:65], v[138:141], v[184:187], v[62:65]
	v_mfma_f32_16x16x32_bf16 v[42:45], v[130:133], v[192:195], v[42:45]
	v_mfma_f32_16x16x32_bf16 v[46:49], v[138:141], v[192:195], v[46:49]
	v_mfma_f32_16x16x32_bf16 v[18:21], v[130:133], v[204:207], v[18:21]
	v_mfma_f32_16x16x32_bf16 v[22:25], v[138:141], v[204:207], v[22:25]
	v_mfma_f32_16x16x32_bf16 v[6:9], v[130:133], v[212:215], v[6:9]
	v_mfma_f32_16x16x32_bf16 v[14:17], v[138:141], v[212:215], v[14:17]
	v_mfma_f32_16x16x32_bf16 v[58:61], v[134:137], v[188:191], v[58:61]
	v_mfma_f32_16x16x32_bf16 v[62:65], v[142:145], v[188:191], v[62:65]
	v_mfma_f32_16x16x32_bf16 v[42:45], v[134:137], v[196:199], v[42:45]
	v_mfma_f32_16x16x32_bf16 v[46:49], v[142:145], v[196:199], v[46:49]
	v_mfma_f32_16x16x32_bf16 v[18:21], v[134:137], v[208:211], v[18:21]
	v_mfma_f32_16x16x32_bf16 v[22:25], v[142:145], v[208:211], v[22:25]
	v_mfma_f32_16x16x32_bf16 v[6:9], v[134:137], v[216:219], v[6:9]
	v_mfma_f32_16x16x32_bf16 v[14:17], v[142:145], v[216:219], v[14:17]
	v_mfma_f32_16x16x32_bf16 v[50:53], v[162:165], v[184:187], v[50:53]
	v_mfma_f32_16x16x32_bf16 v[54:57], v[176:179], v[184:187], v[54:57]
	v_mfma_f32_16x16x32_bf16 v[34:37], v[162:165], v[192:195], v[34:37]
	v_mfma_f32_16x16x32_bf16 v[38:41], v[176:179], v[192:195], v[38:41]
	v_mfma_f32_16x16x32_bf16 v[26:29], v[162:165], v[204:207], v[26:29]
	v_mfma_f32_16x16x32_bf16 v[30:33], v[176:179], v[204:207], v[30:33]
	v_mfma_f32_16x16x32_bf16 v[10:13], v[162:165], v[212:215], v[10:13]
	v_mfma_f32_16x16x32_bf16 v[2:5], v[176:179], v[212:215], v[2:5]
	v_mfma_f32_16x16x32_bf16 v[50:53], v[166:169], v[188:191], v[50:53]
	v_mfma_f32_16x16x32_bf16 v[54:57], v[180:183], v[188:191], v[54:57]
	v_mfma_f32_16x16x32_bf16 v[34:37], v[166:169], v[196:199], v[34:37]
	v_mfma_f32_16x16x32_bf16 v[38:41], v[180:183], v[196:199], v[38:41]
	v_mfma_f32_16x16x32_bf16 v[26:29], v[166:169], v[208:211], v[26:29]
	v_mfma_f32_16x16x32_bf16 v[30:33], v[180:183], v[208:211], v[30:33]
	v_mfma_f32_16x16x32_bf16 v[10:13], v[166:169], v[216:219], v[10:13]
	v_mfma_f32_16x16x32_bf16 v[2:5], v[180:183], v[216:219], v[2:5]
	s_setprio 0
	s_barrier
	s_add_i32 s49, s49, 2
	s_add_u32 s10, s10, 0x100
	s_addc_u32 s11, s11, 0
	s_add_u32 s37, s37, 0x100
	s_addc_u32 s47, s47, 0
	s_cmp_gt_u32 s49, 29
	s_cbranch_scc0 .LBB0_110
	s_and_b64 vcc, exec, s[38:39]
	s_cbranch_vccz .LBB0_113
	s_barrier

; #define PG8_STAGE(bufoff, gbase, voff) do { _Pragma("unroll") for (int _i = 0; _i < 2; ++_i) \
;         __builtin_amdgcn_global_load_lds((const unsigned*)((const char*)(gbase) + (voff)[_i]), (PG8_LAS unsigned*)(lds + (bufoff) + ldsw + _i * 8192), 16, 0, 0); } while (0)
; #define PG8_LDA(dst, b, h) do { _Pragma("unroll") for (int m = 0; m < 4; ++m) _Pragma("unroll") for (int k = 0; k < 2; ++k) dst[m][k] = *(const PG8_LAS bf16x8*)(lds + PG8_SA(b, h) + aoff + m * 2048 + k * 1024); } while (0)
; #define PG8_LDB(dst, b, h) do { _Pragma("unroll") for (int n = 0; n < 2; ++n) _Pragma("unroll") for (int k = 0; k < 2; ++k) dst[n][k] = *(const PG8_LAS bf16x8*)(lds + PG8_SB(b, h) + boff + n * 2048 + k * 1024); } while (0)
; #define PG8_MMA(ai, bj, At, Bt) do { __builtin_amdgcn_s_setprio(1); _Pragma("unroll") for (int m = 0; m < 4; ++m) _Pragma("unroll") for (int n = 0; n < 2; ++n) _Pragma("unroll") for (int k = 0; k < 2; ++k) \
;         acc[ai][bj][m][n] = __builtin_amdgcn_mfma_f32_16x16x32_bf16(Bt[n][k], At[m][k], acc[ai][bj][m][n], 0, 0, 0); __builtin_amdgcn_s_setprio(0); } while (0)
; #define PG8_WAIT_V(n) asm volatile("s_waitcnt vmcnt(" #n ")" ::: "memory")
; #define PG8_WAIT_L(n) asm volatile("s_waitcnt lgkmcnt(" #n ")" ::: "memory")
; template <class Epi, class Sched, bool ALIGN_EPI = false, bool SP2 = false>
; __device__ __forceinline__ void gemm_phase(PG8_LAS unsigned char* lds, const Gemm g, const Sched& S, const Epi& E) {
;     ...
;             const bool last = (t == nt - 2);
;             const char* a1 = cA + (size_t)(t + 1) * kstep;
;             const char* a2 = last ? nA : cA + (size_t)(t + 2) * kstep; const char* b2 = last ? nB : cB + (size_t)(t + 2) * kstep;
;             const char* a3 = a2 + kstep; const char* b3 = b2 + kstep;
;             if (last && has_next) S.a_ready(nxt);
;             if constexpr (SP2) {
;             PG8_LDB(B0, 0, 0); PG8_LDB(B1, 0, 1); PG8_SCHED; PG8_LDA(At, 0, 0); PG8_STAGEA(PG8_SA(1, 1), a1, 1, false);
;             PG8_WAIT_V(8); PG8_WAIT_L(0); PG8_BAR; PG8_MMA(0, 0, At, B0); PG8_MMA(0, 1, At, B1); PG8_BAR; PG8_SCHED;
;             PG8_LDA(At, 0, 1); PG8_STAGE(PG8_SB(0, 0), b2, voffB); PG8_STAGE(PG8_SB(0, 1), b2 + hstep, voffB); PG8_STAGEA(PG8_SA(0, 0), a2, 0, last);
;             PG8_WAIT_V(8); PG8_WAIT_L(0); PG8_BAR; PG8_MMA(1, 0, At, B0); PG8_MMA(1, 1, At, B1); PG8_BAR; PG8_SCHED;
.LBB0_383:
	v_add_u32_e32 v142, s79, v173
	v_add_u32_e32 v170, s80, v173
	ds_read_b128 v[130:133], v142
	ds_read_b128 v[134:137], v142 offset:1024
	ds_read_b128 v[138:141], v142 offset:2048
	ds_read_b128 v[142:145], v142 offset:3072
	ds_read_b128 v[146:149], v170
	ds_read_b128 v[150:153], v170 offset:1024
	ds_read_b128 v[154:157], v170 offset:2048
	ds_read_b128 v[176:179], v170 offset:3072
	s_add_i32 s58, s56, 1
	s_ashr_i32 s59, s58, 31
	s_mov_b32 s62, s56
	s_add_i32 s56, s56, 2
	s_lshl_b64 s[96:97], s[58:59], 7
	s_cmp_eq_u32 s62, 30
	s_cselect_b32 s63, s9, s36
	s_cselect_b32 s62, s49, s19
	s_cselect_b32 s59, s89, s57
	s_cselect_b32 s58, s90, s37
	s_add_u32 s95, s10, s96
	s_addc_u32 s97, s11, s97
	s_add_u32 s96, s95, 0x80000
	s_addc_u32 s97, s97, 0
	v_lshl_add_u64 v[170:171], s[96:97], 0, v[158:159]
	s_add_i32 m0, s66, 0xc000
	ds_read_b128 v[180:183], v174
	ds_read_b128 v[184:187], v174 offset:1024
	ds_read_b128 v[188:191], v174 offset:2048
	ds_read_b128 v[192:195], v174 offset:3072
	ds_read_b128 v[196:199], v174 offset:4096
	ds_read_b128 v[204:207], v174 offset:5120
	ds_read_b128 v[208:211], v174 offset:6144
	ds_read_b128 v[212:215], v174 offset:7168
	global_load_lds_dwordx4 v[170:171], off
	v_lshl_add_u64 v[170:171], s[96:97], 0, v[162:163]
	s_add_i32 m0, s66, 0xe000
	s_nop 0
	global_load_lds_dwordx4 v[170:171], off
	s_waitcnt vmcnt(8) lgkmcnt(0)
	s_barrier
	s_setprio 1
	v_mfma_f32_16x16x32_bf16 v[118:121], v[130:133], v[180:183], v[118:121]
	v_mfma_f32_16x16x32_bf16 v[114:117], v[138:141], v[180:183], v[114:117]
	v_mfma_f32_16x16x32_bf16 v[102:105], v[130:133], v[188:191], v[102:105]
	v_mfma_f32_16x16x32_bf16 v[98:101], v[138:141], v[188:191], v[98:101]
	v_mfma_f32_16x16x32_bf16 v[86:89], v[130:133], v[196:199], v[86:89]
	v_mfma_f32_16x16x32_bf16 v[82:85], v[138:141], v[196:199], v[82:85]
	v_mfma_f32_16x16x32_bf16 v[70:73], v[130:133], v[208:211], v[70:73]
	v_mfma_f32_16x16x32_bf16 v[66:69], v[138:141], v[208:211], v[66:69]
	v_mfma_f32_16x16x32_bf16 v[118:121], v[134:137], v[184:187], v[118:121]
	v_mfma_f32_16x16x32_bf16 v[114:117], v[142:145], v[184:187], v[114:117]
	v_mfma_f32_16x16x32_bf16 v[102:105], v[134:137], v[192:195], v[102:105]
	v_mfma_f32_16x16x32_bf16 v[98:101], v[142:145], v[192:195], v[98:101]
	v_mfma_f32_16x16x32_bf16 v[86:89], v[134:137], v[204:207], v[86:89]
	v_mfma_f32_16x16x32_bf16 v[82:85], v[142:145], v[204:207], v[82:85]
	v_mfma_f32_16x16x32_bf16 v[70:73], v[134:137], v[212:215], v[70:73]
	v_mfma_f32_16x16x32_bf16 v[66:69], v[142:145], v[212:215], v[66:69]
	v_mfma_f32_16x16x32_bf16 v[126:129], v[146:149], v[180:183], v[126:129]
	v_mfma_f32_16x16x32_bf16 v[122:125], v[154:157], v[180:183], v[122:125]
	v_mfma_f32_16x16x32_bf16 v[110:113], v[146:149], v[188:191], v[110:113]
	v_mfma_f32_16x16x32_bf16 v[106:109], v[154:157], v[188:191], v[106:109]
	v_mfma_f32_16x16x32_bf16 v[94:97], v[146:149], v[196:199], v[94:97]
	v_mfma_f32_16x16x32_bf16 v[90:93], v[154:157], v[196:199], v[90:93]
	v_mfma_f32_16x16x32_bf16 v[78:81], v[146:149], v[208:211], v[78:81]
	v_mfma_f32_16x16x32_bf16 v[74:77], v[154:157], v[208:211], v[74:77]
	v_mfma_f32_16x16x32_bf16 v[126:129], v[150:153], v[184:187], v[126:129]
	v_mfma_f32_16x16x32_bf16 v[122:125], v[176:179], v[184:187], v[122:125]
	v_mfma_f32_16x16x32_bf16 v[110:113], v[150:153], v[192:195], v[110:113]
	v_mfma_f32_16x16x32_bf16 v[106:109], v[176:179], v[192:195], v[106:109]
	v_mfma_f32_16x16x32_bf16 v[94:97], v[150:153], v[204:207], v[94:97]
	v_mfma_f32_16x16x32_bf16 v[90:93], v[176:179], v[204:207], v[90:93]
	v_mfma_f32_16x16x32_bf16 v[78:81], v[150:153], v[212:215], v[78:81]
	v_mfma_f32_16x16x32_bf16 v[74:77], v[176:179], v[212:215], v[74:77]
	s_setprio 0
	s_barrier
	s_add_i32 s95, s79, s65
	v_lshl_add_u64 v[170:171], s[58:59], 0, v[160:161]
	s_mov_b32 m0, s95
	ds_read_b128 v[180:183], v174 offset:16384
	ds_read_b128 v[184:187], v174 offset:17408
	ds_read_b128 v[188:191], v174 offset:18432
	ds_read_b128 v[192:195], v174 offset:19456
	ds_read_b128 v[196:199], v174 offset:20480
	ds_read_b128 v[204:207], v174 offset:21504
	ds_read_b128 v[208:211], v174 offset:22528
	ds_read_b128 v[212:215], v174 offset:23552
	global_load_lds_dwordx4 v[170:171], off
	s_add_i32 m0, s95, 0x2000
	s_add_u32 s96, s58, 0x80000
	v_lshl_add_u64 v[200:201], s[58:59], 0, v[164:165]
	s_addc_u32 s97, s59, 0
	s_add_i32 s95, s80, s65
	global_load_lds_dwordx4 v[200:201], off
	v_lshl_add_u64 v[216:217], s[96:97], 0, v[160:161]
	s_mov_b32 m0, s95
	v_lshl_add_u64 v[218:219], s[62:63], 0, v[162:163]
	global_load_lds_dwordx4 v[216:217], off
	v_lshl_add_u64 v[216:217], s[96:97], 0, v[164:165]
	s_add_i32 m0, s95, 0x2000
	s_nop 0
	global_load_lds_dwordx4 v[216:217], off
	v_lshl_add_u64 v[216:217], s[62:63], 0, v[158:159]
	s_mov_b32 m0, s66
	s_nop 0
	global_load_lds_dwordx4 v[216:217], off
	s_mov_b32 m0, s67
	s_nop 0
	global_load_lds_dwordx4 v[218:219], off
	s_waitcnt vmcnt(8) lgkmcnt(0)
	s_barrier
; #define PG8_LDA(dst, b, h) do { _Pragma("unroll") for (int m = 0; m < 4; ++m) _Pragma("unroll") for (int k = 0; k < 2; ++k) dst[m][k] = *(const PG8_LAS bf16x8*)(lds + PG8_SA(b, h) + aoff + m * 2048 + k * 1024); } while (0)
; #define PG8_LDB(dst, b, h) do { _Pragma("unroll") for (int n = 0; n < 2; ++n) _Pragma("unroll") for (int k = 0; k < 2; ++k) dst[n][k] = *(const PG8_LAS bf16x8*)(lds + PG8_SB(b, h) + boff + n * 2048 + k * 1024); } while (0)
; #define PG8_MMA(ai, bj, At, Bt) do { __builtin_amdgcn_s_setprio(1); _Pragma("unroll") for (int m = 0; m < 4; ++m) _Pragma("unroll") for (int n = 0; n < 2; ++n) _Pragma("unroll") for (int k = 0; k < 2; ++k) \
;         acc[ai][bj][m][n] = __builtin_amdgcn_mfma_f32_16x16x32_bf16(Bt[n][k], At[m][k], acc[ai][bj][m][n], 0, 0, 0); __builtin_amdgcn_s_setprio(0); } while (0)
; #define PG8_WAIT_V(n) asm volatile("s_waitcnt vmcnt(" #n ")" ::: "memory")
; #define PG8_WAIT_L(n) asm volatile("s_waitcnt lgkmcnt(" #n ")" ::: "memory")
; #define PG8_BAR __builtin_amdgcn_s_barrier()
; #define PG8_SCHED __builtin_amdgcn_sched_barrier(0)
; template <class Epi, class Sched, bool ALIGN_EPI = false, bool SP2 = false>
; __device__ __forceinline__ void gemm_phase(PG8_LAS unsigned char* lds, const Gemm g, const Sched& S, const Epi& E) {
;     ...
;             PG8_WAIT_V(8); PG8_WAIT_L(0); PG8_BAR; PG8_MMA(1, 0, At, B0); PG8_MMA(1, 1, At, B1); PG8_BAR; PG8_SCHED;
;             PG8_LDB(B0, 1, 0); PG8_LDB(B1, 1, 1); PG8_SCHED; PG8_LDA(At, 1, 0); PG8_STAGEA(PG8_SA(0, 1), a2, 1, last);
;             PG8_WAIT_V(8); PG8_WAIT_L(0); PG8_BAR; PG8_MMA(0, 0, At, B0); PG8_MMA(0, 1, At, B1); PG8_BAR; PG8_SCHED;
	s_setprio 1
	v_mfma_f32_16x16x32_bf16 v[54:57], v[130:133], v[180:183], v[54:57]
	v_mfma_f32_16x16x32_bf16 v[50:53], v[138:141], v[180:183], v[50:53]
	v_mfma_f32_16x16x32_bf16 v[38:41], v[130:133], v[188:191], v[38:41]
	v_mfma_f32_16x16x32_bf16 v[34:37], v[138:141], v[188:191], v[34:37]
	v_mfma_f32_16x16x32_bf16 v[22:25], v[130:133], v[196:199], v[22:25]
	v_mfma_f32_16x16x32_bf16 v[18:21], v[138:141], v[196:199], v[18:21]
	v_mfma_f32_16x16x32_bf16 v[10:13], v[130:133], v[208:211], v[10:13]
	v_mfma_f32_16x16x32_bf16 v[6:9], v[138:141], v[208:211], v[6:9]
	v_mfma_f32_16x16x32_bf16 v[54:57], v[134:137], v[184:187], v[54:57]
	v_mfma_f32_16x16x32_bf16 v[50:53], v[142:145], v[184:187], v[50:53]
	v_mfma_f32_16x16x32_bf16 v[38:41], v[134:137], v[192:195], v[38:41]
	v_mfma_f32_16x16x32_bf16 v[34:37], v[142:145], v[192:195], v[34:37]
	v_mfma_f32_16x16x32_bf16 v[22:25], v[134:137], v[204:207], v[22:25]
	v_mfma_f32_16x16x32_bf16 v[18:21], v[142:145], v[204:207], v[18:21]
	v_mfma_f32_16x16x32_bf16 v[10:13], v[134:137], v[212:215], v[10:13]
	v_mfma_f32_16x16x32_bf16 v[6:9], v[142:145], v[212:215], v[6:9]
	v_mfma_f32_16x16x32_bf16 v[62:65], v[146:149], v[180:183], v[62:65]
	v_mfma_f32_16x16x32_bf16 v[58:61], v[154:157], v[180:183], v[58:61]
	v_mfma_f32_16x16x32_bf16 v[46:49], v[146:149], v[188:191], v[46:49]
	v_mfma_f32_16x16x32_bf16 v[42:45], v[154:157], v[188:191], v[42:45]
	v_mfma_f32_16x16x32_bf16 v[30:33], v[146:149], v[196:199], v[30:33]
	v_mfma_f32_16x16x32_bf16 v[26:29], v[154:157], v[196:199], v[26:29]
	v_mfma_f32_16x16x32_bf16 v[14:17], v[146:149], v[208:211], v[14:17]
	v_mfma_f32_16x16x32_bf16 v[2:5], v[154:157], v[208:211], v[2:5]
	v_mfma_f32_16x16x32_bf16 v[62:65], v[150:153], v[184:187], v[62:65]
	v_mfma_f32_16x16x32_bf16 v[58:61], v[176:179], v[184:187], v[58:61]
	v_mfma_f32_16x16x32_bf16 v[46:49], v[150:153], v[192:195], v[46:49]
	v_mfma_f32_16x16x32_bf16 v[42:45], v[176:179], v[192:195], v[42:45]
	v_mfma_f32_16x16x32_bf16 v[30:33], v[150:153], v[204:207], v[30:33]
	v_mfma_f32_16x16x32_bf16 v[26:29], v[176:179], v[204:207], v[26:29]
	v_mfma_f32_16x16x32_bf16 v[14:17], v[150:153], v[212:215], v[14:17]
	v_mfma_f32_16x16x32_bf16 v[2:5], v[176:179], v[212:215], v[2:5]
	s_setprio 0
	s_barrier
	s_add_i32 s95, 0, 0x18000
	s_add_i32 s96, 0, 0x1c000
	v_add_u32_e32 v142, s95, v173
	v_add_u32_e32 v175, s96, v173
	ds_read_b128 v[130:133], v142
	ds_read_b128 v[134:137], v142 offset:1024
	ds_read_b128 v[138:141], v142 offset:2048
	ds_read_b128 v[142:145], v142 offset:3072
	ds_read_b128 v[146:149], v175
	ds_read_b128 v[150:153], v175 offset:1024
	ds_read_b128 v[154:157], v175 offset:2048
	ds_read_b128 v[176:179], v175 offset:3072
	s_add_u32 s62, s62, 0x80000
	s_addc_u32 s63, s63, 0
	s_mov_b32 m0, s68
	v_lshl_add_u64 v[220:221], s[62:63], 0, v[158:159]
	ds_read_b128 v[180:183], v174 offset:32768
	ds_read_b128 v[184:187], v174 offset:33792
	ds_read_b128 v[188:191], v174 offset:34816
	ds_read_b128 v[192:195], v174 offset:35840
	ds_read_b128 v[196:199], v174 offset:36864
	ds_read_b128 v[204:207], v174 offset:37888
	ds_read_b128 v[208:211], v174 offset:38912
	ds_read_b128 v[212:215], v174 offset:39936
	global_load_lds_dwordx4 v[220:221], off
	v_lshl_add_u64 v[220:221], s[62:63], 0, v[162:163]
	s_mov_b32 m0, s69
	s_nop 0
	global_load_lds_dwordx4 v[220:221], off
	s_waitcnt vmcnt(8) lgkmcnt(0)
	s_barrier
	s_setprio 1
	v_mfma_f32_16x16x32_bf16 v[118:121], v[130:133], v[180:183], v[118:121]
	v_mfma_f32_16x16x32_bf16 v[114:117], v[138:141], v[180:183], v[114:117]
	v_mfma_f32_16x16x32_bf16 v[102:105], v[130:133], v[188:191], v[102:105]
	v_mfma_f32_16x16x32_bf16 v[98:101], v[138:141], v[188:191], v[98:101]
	v_mfma_f32_16x16x32_bf16 v[86:89], v[130:133], v[196:199], v[86:89]
	v_mfma_f32_16x16x32_bf16 v[82:85], v[138:141], v[196:199], v[82:85]
	v_mfma_f32_16x16x32_bf16 v[70:73], v[130:133], v[208:211], v[70:73]
	v_mfma_f32_16x16x32_bf16 v[66:69], v[138:141], v[208:211], v[66:69]
	v_mfma_f32_16x16x32_bf16 v[118:121], v[134:137], v[184:187], v[118:121]
	v_mfma_f32_16x16x32_bf16 v[114:117], v[142:145], v[184:187], v[114:117]
	v_mfma_f32_16x16x32_bf16 v[102:105], v[134:137], v[192:195], v[102:105]
	v_mfma_f32_16x16x32_bf16 v[98:101], v[142:145], v[192:195], v[98:101]
	v_mfma_f32_16x16x32_bf16 v[86:89], v[134:137], v[204:207], v[86:89]
	v_mfma_f32_16x16x32_bf16 v[82:85], v[142:145], v[204:207], v[82:85]
	v_mfma_f32_16x16x32_bf16 v[70:73], v[134:137], v[212:215], v[70:73]
	v_mfma_f32_16x16x32_bf16 v[66:69], v[142:145], v[212:215], v[66:69]
	v_mfma_f32_16x16x32_bf16 v[126:129], v[146:149], v[180:183], v[126:129]
	v_mfma_f32_16x16x32_bf16 v[122:125], v[154:157], v[180:183], v[122:125]
	v_mfma_f32_16x16x32_bf16 v[110:113], v[146:149], v[188:191], v[110:113]
	v_mfma_f32_16x16x32_bf16 v[106:109], v[154:157], v[188:191], v[106:109]
	v_mfma_f32_16x16x32_bf16 v[94:97], v[146:149], v[196:199], v[94:97]
	v_mfma_f32_16x16x32_bf16 v[90:93], v[154:157], v[196:199], v[90:93]
	v_mfma_f32_16x16x32_bf16 v[78:81], v[146:149], v[208:211], v[78:81]
	v_mfma_f32_16x16x32_bf16 v[74:77], v[154:157], v[208:211], v[74:77]
	v_mfma_f32_16x16x32_bf16 v[126:129], v[150:153], v[184:187], v[126:129]
	v_mfma_f32_16x16x32_bf16 v[122:125], v[176:179], v[184:187], v[122:125]
	v_mfma_f32_16x16x32_bf16 v[110:113], v[150:153], v[192:195], v[110:113]
	v_mfma_f32_16x16x32_bf16 v[106:109], v[176:179], v[192:195], v[106:109]
	v_mfma_f32_16x16x32_bf16 v[94:97], v[150:153], v[204:207], v[94:97]
	v_mfma_f32_16x16x32_bf16 v[90:93], v[176:179], v[204:207], v[90:93]
	v_mfma_f32_16x16x32_bf16 v[78:81], v[150:153], v[212:215], v[78:81]
	v_mfma_f32_16x16x32_bf16 v[74:77], v[176:179], v[212:215], v[74:77]
	s_setprio 0
	s_barrier
; #define PG8_STAGE(bufoff, gbase, voff) do { _Pragma("unroll") for (int _i = 0; _i < 2; ++_i) \
;         __builtin_amdgcn_global_load_lds((const unsigned*)((const char*)(gbase) + (voff)[_i]), (PG8_LAS unsigned*)(lds + (bufoff) + ldsw + _i * 8192), 16, 0, 0); } while (0)
; #define PG8_LDA(dst, b, h) do { _Pragma("unroll") for (int m = 0; m < 4; ++m) _Pragma("unroll") for (int k = 0; k < 2; ++k) dst[m][k] = *(const PG8_LAS bf16x8*)(lds + PG8_SA(b, h) + aoff + m * 2048 + k * 1024); } while (0)
; #define PG8_MMA(ai, bj, At, Bt) do { __builtin_amdgcn_s_setprio(1); _Pragma("unroll") for (int m = 0; m < 4; ++m) _Pragma("unroll") for (int n = 0; n < 2; ++n) _Pragma("unroll") for (int k = 0; k < 2; ++k) \
;         acc[ai][bj][m][n] = __builtin_amdgcn_mfma_f32_16x16x32_bf16(Bt[n][k], At[m][k], acc[ai][bj][m][n], 0, 0, 0); __builtin_amdgcn_s_setprio(0); } while (0)
; #define PG8_WAIT_V(n) asm volatile("s_waitcnt vmcnt(" #n ")" ::: "memory")
; #define PG8_WAIT_L(n) asm volatile("s_waitcnt lgkmcnt(" #n ")" ::: "memory")
; #define PG8_BAR __builtin_amdgcn_s_barrier()
; #define PG8_SCHED __builtin_amdgcn_sched_barrier(0)
; template <class Epi, class Sched, bool ALIGN_EPI = false, bool SP2 = false>
; __device__ __forceinline__ void gemm_phase(PG8_LAS unsigned char* lds, const Gemm g, const Sched& S, const Epi& E) {
;     ...
;             PG8_LDA(At, 1, 1); PG8_STAGE(PG8_SB(1, 0), b3, voffB); PG8_STAGE(PG8_SB(1, 1), b3 + hstep, voffB); PG8_STAGEA(PG8_SA(1, 0), a3, 0, last);
;             PG8_WAIT_V(8); PG8_WAIT_L(0); PG8_BAR; PG8_MMA(1, 0, At, B0); PG8_MMA(1, 1, At, B1); PG8_BAR; PG8_SCHED;
	s_add_i32 s62, s95, s65
	v_lshl_add_u64 v[170:171], v[170:171], 0, s[26:27]
	s_mov_b32 m0, s62
	ds_read_b128 v[180:183], v174 offset:49152
	ds_read_b128 v[184:187], v174 offset:50176
	ds_read_b128 v[188:191], v174 offset:51200
	ds_read_b128 v[192:195], v174 offset:52224
	ds_read_b128 v[196:199], v174 offset:53248
	ds_read_b128 v[204:207], v174 offset:54272
	ds_read_b128 v[208:211], v174 offset:55296
	ds_read_b128 v[212:215], v174 offset:56320
	global_load_lds_dwordx4 v[170:171], off
	s_add_i32 m0, s62, 0x2000
	s_add_u32 s58, s58, 0x80080
	v_lshl_add_u64 v[170:171], v[200:201], 0, s[26:27]
	s_addc_u32 s59, s59, 0
	s_add_i32 s62, s96, s65
	global_load_lds_dwordx4 v[170:171], off
	v_lshl_add_u64 v[170:171], s[58:59], 0, v[160:161]
	s_mov_b32 m0, s62
	s_nop 0
	global_load_lds_dwordx4 v[170:171], off
	v_lshl_add_u64 v[170:171], s[58:59], 0, v[164:165]
	s_add_i32 m0, s62, 0x2000
	s_nop 0
	global_load_lds_dwordx4 v[170:171], off
	v_lshl_add_u64 v[170:171], v[216:217], 0, s[26:27]
	s_mov_b32 m0, s76
	s_nop 0
	global_load_lds_dwordx4 v[170:171], off
	v_lshl_add_u64 v[170:171], v[218:219], 0, s[26:27]
	s_mov_b32 m0, s77
	s_nop 0
	global_load_lds_dwordx4 v[170:171], off
	s_waitcnt vmcnt(8) lgkmcnt(0)
	s_barrier
	s_setprio 1
	v_mfma_f32_16x16x32_bf16 v[54:57], v[130:133], v[180:183], v[54:57]
	v_mfma_f32_16x16x32_bf16 v[50:53], v[138:141], v[180:183], v[50:53]
	v_mfma_f32_16x16x32_bf16 v[38:41], v[130:133], v[188:191], v[38:41]
	v_mfma_f32_16x16x32_bf16 v[34:37], v[138:141], v[188:191], v[34:37]
	v_mfma_f32_16x16x32_bf16 v[22:25], v[130:133], v[196:199], v[22:25]
	v_mfma_f32_16x16x32_bf16 v[18:21], v[138:141], v[196:199], v[18:21]
	v_mfma_f32_16x16x32_bf16 v[10:13], v[130:133], v[208:211], v[10:13]
	v_mfma_f32_16x16x32_bf16 v[6:9], v[138:141], v[208:211], v[6:9]
	v_mfma_f32_16x16x32_bf16 v[54:57], v[134:137], v[184:187], v[54:57]
	v_mfma_f32_16x16x32_bf16 v[50:53], v[142:145], v[184:187], v[50:53]
	v_mfma_f32_16x16x32_bf16 v[38:41], v[134:137], v[192:195], v[38:41]
	v_mfma_f32_16x16x32_bf16 v[34:37], v[142:145], v[192:195], v[34:37]
	v_mfma_f32_16x16x32_bf16 v[22:25], v[134:137], v[204:207], v[22:25]
	v_mfma_f32_16x16x32_bf16 v[18:21], v[142:145], v[204:207], v[18:21]
	v_mfma_f32_16x16x32_bf16 v[10:13], v[134:137], v[212:215], v[10:13]
	v_mfma_f32_16x16x32_bf16 v[6:9], v[142:145], v[212:215], v[6:9]
	v_mfma_f32_16x16x32_bf16 v[62:65], v[146:149], v[180:183], v[62:65]
	v_mfma_f32_16x16x32_bf16 v[58:61], v[154:157], v[180:183], v[58:61]
	v_mfma_f32_16x16x32_bf16 v[46:49], v[146:149], v[188:191], v[46:49]
	v_mfma_f32_16x16x32_bf16 v[42:45], v[154:157], v[188:191], v[42:45]
	v_mfma_f32_16x16x32_bf16 v[30:33], v[146:149], v[196:199], v[30:33]
	v_mfma_f32_16x16x32_bf16 v[26:29], v[154:157], v[196:199], v[26:29]
	v_mfma_f32_16x16x32_bf16 v[14:17], v[146:149], v[208:211], v[14:17]
	v_mfma_f32_16x16x32_bf16 v[2:5], v[154:157], v[208:211], v[2:5]
	v_mfma_f32_16x16x32_bf16 v[62:65], v[150:153], v[184:187], v[62:65]
	v_mfma_f32_16x16x32_bf16 v[58:61], v[176:179], v[184:187], v[58:61]
	v_mfma_f32_16x16x32_bf16 v[46:49], v[150:153], v[192:195], v[46:49]
	v_mfma_f32_16x16x32_bf16 v[42:45], v[176:179], v[192:195], v[42:45]
	v_mfma_f32_16x16x32_bf16 v[30:33], v[150:153], v[204:207], v[30:33]
	v_mfma_f32_16x16x32_bf16 v[26:29], v[176:179], v[204:207], v[26:29]
	v_mfma_f32_16x16x32_bf16 v[14:17], v[150:153], v[212:215], v[14:17]
	v_mfma_f32_16x16x32_bf16 v[2:5], v[176:179], v[212:215], v[2:5]
	s_setprio 0
	s_barrier
	s_add_u32 s19, s19, 0x100
	s_addc_u32 s36, s36, 0
	s_add_u32 s37, s37, 0x100
	s_addc_u32 s57, s57, 0
	s_cmp_lt_i32 s56, s18
	s_cbranch_scc1 .LBB0_383

; #define PG8_STAGE(bufoff, gbase, voff) do { _Pragma("unroll") for (int _i = 0; _i < 2; ++_i) \
;         __builtin_amdgcn_global_load_lds((const unsigned*)((const char*)(gbase) + (voff)[_i]), (PG8_LAS unsigned*)(lds + (bufoff) + ldsw + _i * 8192), 16, 0, 0); } while (0)
; #define PG8_LDA(dst, b, h) do { _Pragma("unroll") for (int m = 0; m < 4; ++m) _Pragma("unroll") for (int k = 0; k < 2; ++k) dst[m][k] = *(const PG8_LAS bf16x8*)(lds + PG8_SA(b, h) + aoff + m * 2048 + k * 1024); } while (0)
; #define PG8_LDB(dst, b, h) do { _Pragma("unroll") for (int n = 0; n < 2; ++n) _Pragma("unroll") for (int k = 0; k < 2; ++k) dst[n][k] = *(const PG8_LAS bf16x8*)(lds + PG8_SB(b, h) + boff + n * 2048 + k * 1024); } while (0)
; #define PG8_MMA(ai, bj, At, Bt) do { __builtin_amdgcn_s_setprio(1); _Pragma("unroll") for (int m = 0; m < 4; ++m) _Pragma("unroll") for (int n = 0; n < 2; ++n) _Pragma("unroll") for (int k = 0; k < 2; ++k) \
;         acc[ai][bj][m][n] = __builtin_amdgcn_mfma_f32_16x16x32_bf16(Bt[n][k], At[m][k], acc[ai][bj][m][n], 0, 0, 0); __builtin_amdgcn_s_setprio(0); } while (0)
; #define PG8_WAIT_V(n) asm volatile("s_waitcnt vmcnt(" #n ")" ::: "memory")
; #define PG8_WAIT_L(n) asm volatile("s_waitcnt lgkmcnt(" #n ")" ::: "memory")
; template <class Epi, class Sched, bool ALIGN_EPI = false, bool SP2 = false>
; __device__ __forceinline__ void gemm_phase(PG8_LAS unsigned char* lds, const Gemm g, const Sched& S, const Epi& E) {
;     ...
;             const bool last = (t == nt - 2);
;             const char* a1 = cA + (size_t)(t + 1) * kstep;
;             const char* a2 = last ? nA : cA + (size_t)(t + 2) * kstep; const char* b2 = last ? nB : cB + (size_t)(t + 2) * kstep;
;             const char* a3 = a2 + kstep; const char* b3 = b2 + kstep;
;             if (last && has_next) S.a_ready(nxt);
;             if constexpr (SP2) {
;             PG8_LDB(B0, 0, 0); PG8_LDB(B1, 0, 1); PG8_SCHED; PG8_LDA(At, 0, 0); PG8_STAGEA(PG8_SA(1, 1), a1, 1, false);
;             PG8_WAIT_V(8); PG8_WAIT_L(0); PG8_BAR; PG8_MMA(0, 0, At, B0); PG8_MMA(0, 1, At, B1); PG8_BAR; PG8_SCHED;
;             PG8_LDA(At, 0, 1); PG8_STAGE(PG8_SB(0, 0), b2, voffB); PG8_STAGE(PG8_SB(0, 1), b2 + hstep, voffB); PG8_STAGEA(PG8_SA(0, 0), a2, 0, last);
;             PG8_WAIT_V(8); PG8_WAIT_L(0); PG8_BAR; PG8_MMA(1, 0, At, B0); PG8_MMA(1, 1, At, B1); PG8_BAR; PG8_SCHED;
.LBB0_571:
	v_add_u32_e32 v162, s66, v150
	v_add_u32_e32 v178, s67, v150
	ds_read_b128 v[146:149], v162
	ds_read_b128 v[154:157], v162 offset:1024
	ds_read_b128 v[158:161], v162 offset:2048
	ds_read_b128 v[162:165], v162 offset:3072
	ds_read_b128 v[166:169], v178
	ds_read_b128 v[170:173], v178 offset:1024
	ds_read_b128 v[174:177], v178 offset:2048
	ds_read_b128 v[178:181], v178 offset:3072
	s_add_u32 s52, s50, 0xfff80080
	s_addc_u32 s53, s51, -1
	s_cmp_eq_u32 s49, 28
	s_cselect_b32 s55, s9, s53
	s_cselect_b32 s54, s11, s52
	s_cselect_b32 s53, s36, s43
	s_cselect_b32 s52, s37, s41
	v_lshl_add_u64 v[216:217], s[50:51], 0, v[138:139]
	s_add_i32 m0, s57, 0xc000
	ds_read_b128 v[182:185], v152
	ds_read_b128 v[186:189], v152 offset:1024
	ds_read_b128 v[190:193], v152 offset:2048
	ds_read_b128 v[194:197], v152 offset:3072
	ds_read_b128 v[198:201], v152 offset:4096
	ds_read_b128 v[204:207], v152 offset:5120
	ds_read_b128 v[208:211], v152 offset:6144
	ds_read_b128 v[212:215], v152 offset:7168
	global_load_lds_dwordx4 v[216:217], off
	v_lshl_add_u64 v[216:217], s[50:51], 0, v[140:141]
	s_add_i32 m0, s57, 0xe000
	s_nop 0
	global_load_lds_dwordx4 v[216:217], off
	s_waitcnt vmcnt(8) lgkmcnt(0)
	s_barrier
	s_setprio 1
	v_mfma_f32_16x16x32_bf16 v[126:129], v[146:149], v[182:185], v[126:129]
	v_mfma_f32_16x16x32_bf16 v[122:125], v[158:161], v[182:185], v[122:125]
	v_mfma_f32_16x16x32_bf16 v[110:113], v[146:149], v[190:193], v[110:113]
	v_mfma_f32_16x16x32_bf16 v[106:109], v[158:161], v[190:193], v[106:109]
	v_mfma_f32_16x16x32_bf16 v[94:97], v[146:149], v[198:201], v[94:97]
	v_mfma_f32_16x16x32_bf16 v[90:93], v[158:161], v[198:201], v[90:93]
	v_mfma_f32_16x16x32_bf16 v[78:81], v[146:149], v[208:211], v[78:81]
	v_mfma_f32_16x16x32_bf16 v[74:77], v[158:161], v[208:211], v[74:77]
	v_mfma_f32_16x16x32_bf16 v[126:129], v[154:157], v[186:189], v[126:129]
	v_mfma_f32_16x16x32_bf16 v[122:125], v[162:165], v[186:189], v[122:125]
	v_mfma_f32_16x16x32_bf16 v[110:113], v[154:157], v[194:197], v[110:113]
	v_mfma_f32_16x16x32_bf16 v[106:109], v[162:165], v[194:197], v[106:109]
	v_mfma_f32_16x16x32_bf16 v[94:97], v[154:157], v[204:207], v[94:97]
	v_mfma_f32_16x16x32_bf16 v[90:93], v[162:165], v[204:207], v[90:93]
	v_mfma_f32_16x16x32_bf16 v[78:81], v[154:157], v[212:215], v[78:81]
	v_mfma_f32_16x16x32_bf16 v[74:77], v[162:165], v[212:215], v[74:77]
	v_mfma_f32_16x16x32_bf16 v[118:121], v[166:169], v[182:185], v[118:121]
	v_mfma_f32_16x16x32_bf16 v[114:117], v[174:177], v[182:185], v[114:117]
	v_mfma_f32_16x16x32_bf16 v[102:105], v[166:169], v[190:193], v[102:105]
	v_mfma_f32_16x16x32_bf16 v[98:101], v[174:177], v[190:193], v[98:101]
	v_mfma_f32_16x16x32_bf16 v[86:89], v[166:169], v[198:201], v[86:89]
	v_mfma_f32_16x16x32_bf16 v[82:85], v[174:177], v[198:201], v[82:85]
	v_mfma_f32_16x16x32_bf16 v[70:73], v[166:169], v[208:211], v[70:73]
	v_mfma_f32_16x16x32_bf16 v[66:69], v[174:177], v[208:211], v[66:69]
	v_mfma_f32_16x16x32_bf16 v[118:121], v[170:173], v[186:189], v[118:121]
	v_mfma_f32_16x16x32_bf16 v[114:117], v[178:181], v[186:189], v[114:117]
	v_mfma_f32_16x16x32_bf16 v[102:105], v[170:173], v[194:197], v[102:105]
	v_mfma_f32_16x16x32_bf16 v[98:101], v[178:181], v[194:197], v[98:101]
	v_mfma_f32_16x16x32_bf16 v[86:89], v[170:173], v[204:207], v[86:89]
	v_mfma_f32_16x16x32_bf16 v[82:85], v[178:181], v[204:207], v[82:85]
	v_mfma_f32_16x16x32_bf16 v[70:73], v[170:173], v[212:215], v[70:73]
	v_mfma_f32_16x16x32_bf16 v[66:69], v[178:181], v[212:215], v[66:69]
	s_setprio 0
	s_barrier
	s_add_i32 s69, s66, s56
	v_lshl_add_u64 v[216:217], s[52:53], 0, v[132:133]
	s_mov_b32 m0, s69
	ds_read_b128 v[182:185], v152 offset:16384
	ds_read_b128 v[186:189], v152 offset:17408
	ds_read_b128 v[190:193], v152 offset:18432
	ds_read_b128 v[194:197], v152 offset:19456
	ds_read_b128 v[198:201], v152 offset:20480
	ds_read_b128 v[204:207], v152 offset:21504
	ds_read_b128 v[208:211], v152 offset:22528
	ds_read_b128 v[212:215], v152 offset:23552
	global_load_lds_dwordx4 v[216:217], off
	s_add_i32 m0, s69, 0x2000
	s_add_u32 s74, s52, 0x80000
	v_lshl_add_u64 v[218:219], s[52:53], 0, v[136:137]
	s_addc_u32 s75, s53, 0
	s_add_i32 s69, s67, s56
	global_load_lds_dwordx4 v[218:219], off
	v_lshl_add_u64 v[220:221], s[74:75], 0, v[132:133]
	s_mov_b32 m0, s69
	v_lshl_add_u64 v[222:223], s[54:55], 0, v[134:135]
	global_load_lds_dwordx4 v[220:221], off
	v_lshl_add_u64 v[220:221], s[74:75], 0, v[136:137]
	s_add_i32 m0, s69, 0x2000
	s_nop 0
	global_load_lds_dwordx4 v[220:221], off
	v_lshl_add_u64 v[220:221], s[54:55], 0, v[130:131]
	s_mov_b32 m0, s57
	s_nop 0
	global_load_lds_dwordx4 v[220:221], off
	s_mov_b32 m0, s58
	s_nop 0
	global_load_lds_dwordx4 v[222:223], off
	s_waitcnt vmcnt(8) lgkmcnt(0)
	s_barrier
; #define PG8_LDA(dst, b, h) do { _Pragma("unroll") for (int m = 0; m < 4; ++m) _Pragma("unroll") for (int k = 0; k < 2; ++k) dst[m][k] = *(const PG8_LAS bf16x8*)(lds + PG8_SA(b, h) + aoff + m * 2048 + k * 1024); } while (0)
; #define PG8_LDB(dst, b, h) do { _Pragma("unroll") for (int n = 0; n < 2; ++n) _Pragma("unroll") for (int k = 0; k < 2; ++k) dst[n][k] = *(const PG8_LAS bf16x8*)(lds + PG8_SB(b, h) + boff + n * 2048 + k * 1024); } while (0)
; #define PG8_MMA(ai, bj, At, Bt) do { __builtin_amdgcn_s_setprio(1); _Pragma("unroll") for (int m = 0; m < 4; ++m) _Pragma("unroll") for (int n = 0; n < 2; ++n) _Pragma("unroll") for (int k = 0; k < 2; ++k) \
;         acc[ai][bj][m][n] = __builtin_amdgcn_mfma_f32_16x16x32_bf16(Bt[n][k], At[m][k], acc[ai][bj][m][n], 0, 0, 0); __builtin_amdgcn_s_setprio(0); } while (0)
; #define PG8_WAIT_V(n) asm volatile("s_waitcnt vmcnt(" #n ")" ::: "memory")
; #define PG8_WAIT_L(n) asm volatile("s_waitcnt lgkmcnt(" #n ")" ::: "memory")
; #define PG8_BAR __builtin_amdgcn_s_barrier()
; #define PG8_SCHED __builtin_amdgcn_sched_barrier(0)
; template <class Epi, class Sched, bool ALIGN_EPI = false, bool SP2 = false>
; __device__ __forceinline__ void gemm_phase(PG8_LAS unsigned char* lds, const Gemm g, const Sched& S, const Epi& E) {
;     ...
;             PG8_WAIT_V(8); PG8_WAIT_L(0); PG8_BAR; PG8_MMA(1, 0, At, B0); PG8_MMA(1, 1, At, B1); PG8_BAR; PG8_SCHED;
;             PG8_LDB(B0, 1, 0); PG8_LDB(B1, 1, 1); PG8_SCHED; PG8_LDA(At, 1, 0); PG8_STAGEA(PG8_SA(0, 1), a2, 1, last);
;             PG8_WAIT_V(8); PG8_WAIT_L(0); PG8_BAR; PG8_MMA(0, 0, At, B0); PG8_MMA(0, 1, At, B1); PG8_BAR; PG8_SCHED;
	s_setprio 1
	v_mfma_f32_16x16x32_bf16 v[62:65], v[146:149], v[182:185], v[62:65]
	v_mfma_f32_16x16x32_bf16 v[58:61], v[158:161], v[182:185], v[58:61]
	v_mfma_f32_16x16x32_bf16 v[46:49], v[146:149], v[190:193], v[46:49]
	v_mfma_f32_16x16x32_bf16 v[42:45], v[158:161], v[190:193], v[42:45]
	v_mfma_f32_16x16x32_bf16 v[30:33], v[146:149], v[198:201], v[30:33]
	v_mfma_f32_16x16x32_bf16 v[26:29], v[158:161], v[198:201], v[26:29]
	v_mfma_f32_16x16x32_bf16 v[14:17], v[146:149], v[208:211], v[14:17]
	v_mfma_f32_16x16x32_bf16 v[10:13], v[158:161], v[208:211], v[10:13]
	v_mfma_f32_16x16x32_bf16 v[62:65], v[154:157], v[186:189], v[62:65]
	v_mfma_f32_16x16x32_bf16 v[58:61], v[162:165], v[186:189], v[58:61]
	v_mfma_f32_16x16x32_bf16 v[46:49], v[154:157], v[194:197], v[46:49]
	v_mfma_f32_16x16x32_bf16 v[42:45], v[162:165], v[194:197], v[42:45]
	v_mfma_f32_16x16x32_bf16 v[30:33], v[154:157], v[204:207], v[30:33]
	v_mfma_f32_16x16x32_bf16 v[26:29], v[162:165], v[204:207], v[26:29]
	v_mfma_f32_16x16x32_bf16 v[14:17], v[154:157], v[212:215], v[14:17]
	v_mfma_f32_16x16x32_bf16 v[10:13], v[162:165], v[212:215], v[10:13]
	v_mfma_f32_16x16x32_bf16 v[54:57], v[166:169], v[182:185], v[54:57]
	v_mfma_f32_16x16x32_bf16 v[50:53], v[174:177], v[182:185], v[50:53]
	v_mfma_f32_16x16x32_bf16 v[38:41], v[166:169], v[190:193], v[38:41]
	v_mfma_f32_16x16x32_bf16 v[34:37], v[174:177], v[190:193], v[34:37]
	v_mfma_f32_16x16x32_bf16 v[22:25], v[166:169], v[198:201], v[22:25]
	v_mfma_f32_16x16x32_bf16 v[18:21], v[174:177], v[198:201], v[18:21]
	v_mfma_f32_16x16x32_bf16 v[6:9], v[166:169], v[208:211], v[6:9]
	v_mfma_f32_16x16x32_bf16 v[2:5], v[174:177], v[208:211], v[2:5]
	v_mfma_f32_16x16x32_bf16 v[54:57], v[170:173], v[186:189], v[54:57]
	v_mfma_f32_16x16x32_bf16 v[50:53], v[178:181], v[186:189], v[50:53]
	v_mfma_f32_16x16x32_bf16 v[38:41], v[170:173], v[194:197], v[38:41]
	v_mfma_f32_16x16x32_bf16 v[34:37], v[178:181], v[194:197], v[34:37]
	v_mfma_f32_16x16x32_bf16 v[22:25], v[170:173], v[204:207], v[22:25]
	v_mfma_f32_16x16x32_bf16 v[18:21], v[178:181], v[204:207], v[18:21]
	v_mfma_f32_16x16x32_bf16 v[6:9], v[170:173], v[212:215], v[6:9]
	v_mfma_f32_16x16x32_bf16 v[2:5], v[178:181], v[212:215], v[2:5]
	s_setprio 0
	s_barrier
	s_add_i32 s69, 0, 0x18000
	s_add_i32 s74, 0, 0x1c000
	v_add_u32_e32 v162, s69, v150
	v_add_u32_e32 v178, s74, v150
	ds_read_b128 v[146:149], v162
	ds_read_b128 v[154:157], v162 offset:1024
	ds_read_b128 v[158:161], v162 offset:2048
	ds_read_b128 v[162:165], v162 offset:3072
	ds_read_b128 v[166:169], v178
	ds_read_b128 v[170:173], v178 offset:1024
	ds_read_b128 v[174:177], v178 offset:2048
	ds_read_b128 v[178:181], v178 offset:3072
	s_add_u32 s54, s54, 0x80000
	s_addc_u32 s55, s55, 0
	s_mov_b32 m0, s59
	v_lshl_add_u64 v[224:225], s[54:55], 0, v[130:131]
	ds_read_b128 v[182:185], v152 offset:32768
	ds_read_b128 v[186:189], v152 offset:33792
	ds_read_b128 v[190:193], v152 offset:34816
	ds_read_b128 v[194:197], v152 offset:35840
	ds_read_b128 v[198:201], v152 offset:36864
	ds_read_b128 v[204:207], v152 offset:37888
	ds_read_b128 v[208:211], v152 offset:38912
	ds_read_b128 v[212:215], v152 offset:39936
	global_load_lds_dwordx4 v[224:225], off
	v_lshl_add_u64 v[224:225], s[54:55], 0, v[134:135]
	s_mov_b32 m0, s60
	s_nop 0
	global_load_lds_dwordx4 v[224:225], off
	s_waitcnt vmcnt(8) lgkmcnt(0)
	s_barrier
	s_setprio 1
	v_mfma_f32_16x16x32_bf16 v[126:129], v[146:149], v[182:185], v[126:129]
	v_mfma_f32_16x16x32_bf16 v[122:125], v[158:161], v[182:185], v[122:125]
	v_mfma_f32_16x16x32_bf16 v[110:113], v[146:149], v[190:193], v[110:113]
	v_mfma_f32_16x16x32_bf16 v[106:109], v[158:161], v[190:193], v[106:109]
	v_mfma_f32_16x16x32_bf16 v[94:97], v[146:149], v[198:201], v[94:97]
	v_mfma_f32_16x16x32_bf16 v[90:93], v[158:161], v[198:201], v[90:93]
	v_mfma_f32_16x16x32_bf16 v[78:81], v[146:149], v[208:211], v[78:81]
	v_mfma_f32_16x16x32_bf16 v[74:77], v[158:161], v[208:211], v[74:77]
	v_mfma_f32_16x16x32_bf16 v[126:129], v[154:157], v[186:189], v[126:129]
	v_mfma_f32_16x16x32_bf16 v[122:125], v[162:165], v[186:189], v[122:125]
	v_mfma_f32_16x16x32_bf16 v[110:113], v[154:157], v[194:197], v[110:113]
	v_mfma_f32_16x16x32_bf16 v[106:109], v[162:165], v[194:197], v[106:109]
	v_mfma_f32_16x16x32_bf16 v[94:97], v[154:157], v[204:207], v[94:97]
	v_mfma_f32_16x16x32_bf16 v[90:93], v[162:165], v[204:207], v[90:93]
	v_mfma_f32_16x16x32_bf16 v[78:81], v[154:157], v[212:215], v[78:81]
	v_mfma_f32_16x16x32_bf16 v[74:77], v[162:165], v[212:215], v[74:77]
	v_mfma_f32_16x16x32_bf16 v[118:121], v[166:169], v[182:185], v[118:121]
	v_mfma_f32_16x16x32_bf16 v[114:117], v[174:177], v[182:185], v[114:117]
	v_mfma_f32_16x16x32_bf16 v[102:105], v[166:169], v[190:193], v[102:105]
	v_mfma_f32_16x16x32_bf16 v[98:101], v[174:177], v[190:193], v[98:101]
	v_mfma_f32_16x16x32_bf16 v[86:89], v[166:169], v[198:201], v[86:89]
	v_mfma_f32_16x16x32_bf16 v[82:85], v[174:177], v[198:201], v[82:85]
	v_mfma_f32_16x16x32_bf16 v[70:73], v[166:169], v[208:211], v[70:73]
	v_mfma_f32_16x16x32_bf16 v[66:69], v[174:177], v[208:211], v[66:69]
	v_mfma_f32_16x16x32_bf16 v[118:121], v[170:173], v[186:189], v[118:121]
	v_mfma_f32_16x16x32_bf16 v[114:117], v[178:181], v[186:189], v[114:117]
	v_mfma_f32_16x16x32_bf16 v[102:105], v[170:173], v[194:197], v[102:105]
	v_mfma_f32_16x16x32_bf16 v[98:101], v[178:181], v[194:197], v[98:101]
	v_mfma_f32_16x16x32_bf16 v[86:89], v[170:173], v[204:207], v[86:89]
	v_mfma_f32_16x16x32_bf16 v[82:85], v[178:181], v[204:207], v[82:85]
	v_mfma_f32_16x16x32_bf16 v[70:73], v[170:173], v[212:215], v[70:73]
	v_mfma_f32_16x16x32_bf16 v[66:69], v[178:181], v[212:215], v[66:69]
	s_setprio 0
	s_barrier
; #define PG8_STAGE(bufoff, gbase, voff) do { _Pragma("unroll") for (int _i = 0; _i < 2; ++_i) \
;         __builtin_amdgcn_global_load_lds((const unsigned*)((const char*)(gbase) + (voff)[_i]), (PG8_LAS unsigned*)(lds + (bufoff) + ldsw + _i * 8192), 16, 0, 0); } while (0)
; #define PG8_LDA(dst, b, h) do { _Pragma("unroll") for (int m = 0; m < 4; ++m) _Pragma("unroll") for (int k = 0; k < 2; ++k) dst[m][k] = *(const PG8_LAS bf16x8*)(lds + PG8_SA(b, h) + aoff + m * 2048 + k * 1024); } while (0)
; #define PG8_MMA(ai, bj, At, Bt) do { __builtin_amdgcn_s_setprio(1); _Pragma("unroll") for (int m = 0; m < 4; ++m) _Pragma("unroll") for (int n = 0; n < 2; ++n) _Pragma("unroll") for (int k = 0; k < 2; ++k) \
;         acc[ai][bj][m][n] = __builtin_amdgcn_mfma_f32_16x16x32_bf16(Bt[n][k], At[m][k], acc[ai][bj][m][n], 0, 0, 0); __builtin_amdgcn_s_setprio(0); } while (0)
; #define PG8_WAIT_V(n) asm volatile("s_waitcnt vmcnt(" #n ")" ::: "memory")
; #define PG8_WAIT_L(n) asm volatile("s_waitcnt lgkmcnt(" #n ")" ::: "memory")
; #define PG8_BAR __builtin_amdgcn_s_barrier()
; #define PG8_SCHED __builtin_amdgcn_sched_barrier(0)
; template <class Epi, class Sched, bool ALIGN_EPI = false, bool SP2 = false>
; __device__ __forceinline__ void gemm_phase(PG8_LAS unsigned char* lds, const Gemm g, const Sched& S, const Epi& E) {
;     ...
;             PG8_LDA(At, 1, 1); PG8_STAGE(PG8_SB(1, 0), b3, voffB); PG8_STAGE(PG8_SB(1, 1), b3 + hstep, voffB); PG8_STAGEA(PG8_SA(1, 0), a3, 0, last);
;             PG8_WAIT_V(8); PG8_WAIT_L(0); PG8_BAR; PG8_MMA(1, 0, At, B0); PG8_MMA(1, 1, At, B1); PG8_BAR; PG8_SCHED;
	s_add_i32 s54, s69, s56
	v_lshl_add_u64 v[216:217], v[216:217], 0, s[26:27]
	s_mov_b32 m0, s54
	ds_read_b128 v[182:185], v152 offset:49152
	ds_read_b128 v[186:189], v152 offset:50176
	ds_read_b128 v[190:193], v152 offset:51200
	ds_read_b128 v[194:197], v152 offset:52224
	ds_read_b128 v[198:201], v152 offset:53248
	ds_read_b128 v[204:207], v152 offset:54272
	ds_read_b128 v[208:211], v152 offset:55296
	ds_read_b128 v[212:215], v152 offset:56320
	global_load_lds_dwordx4 v[216:217], off
	s_add_i32 m0, s54, 0x2000
	s_add_u32 s52, s52, 0x80080
	v_lshl_add_u64 v[216:217], v[218:219], 0, s[26:27]
	s_addc_u32 s53, s53, 0
	s_add_i32 s54, s74, s56
	global_load_lds_dwordx4 v[216:217], off
	v_lshl_add_u64 v[216:217], s[52:53], 0, v[132:133]
	s_mov_b32 m0, s54
	s_nop 0
	global_load_lds_dwordx4 v[216:217], off
	v_lshl_add_u64 v[216:217], s[52:53], 0, v[136:137]
	s_add_i32 m0, s54, 0x2000
	s_nop 0
	global_load_lds_dwordx4 v[216:217], off
	v_lshl_add_u64 v[216:217], v[220:221], 0, s[26:27]
	s_mov_b32 m0, s62
	s_nop 0
	global_load_lds_dwordx4 v[216:217], off
	v_lshl_add_u64 v[216:217], v[222:223], 0, s[26:27]
	s_mov_b32 m0, s63
	s_nop 0
	global_load_lds_dwordx4 v[216:217], off
	s_waitcnt vmcnt(8) lgkmcnt(0)
	s_barrier
	s_setprio 1
	v_mfma_f32_16x16x32_bf16 v[62:65], v[146:149], v[182:185], v[62:65]
	v_mfma_f32_16x16x32_bf16 v[58:61], v[158:161], v[182:185], v[58:61]
	v_mfma_f32_16x16x32_bf16 v[46:49], v[146:149], v[190:193], v[46:49]
	v_mfma_f32_16x16x32_bf16 v[42:45], v[158:161], v[190:193], v[42:45]
	v_mfma_f32_16x16x32_bf16 v[30:33], v[146:149], v[198:201], v[30:33]
	v_mfma_f32_16x16x32_bf16 v[26:29], v[158:161], v[198:201], v[26:29]
	v_mfma_f32_16x16x32_bf16 v[14:17], v[146:149], v[208:211], v[14:17]
	v_mfma_f32_16x16x32_bf16 v[10:13], v[158:161], v[208:211], v[10:13]
	v_mfma_f32_16x16x32_bf16 v[62:65], v[154:157], v[186:189], v[62:65]
	v_mfma_f32_16x16x32_bf16 v[58:61], v[162:165], v[186:189], v[58:61]
	v_mfma_f32_16x16x32_bf16 v[46:49], v[154:157], v[194:197], v[46:49]
	v_mfma_f32_16x16x32_bf16 v[42:45], v[162:165], v[194:197], v[42:45]
	v_mfma_f32_16x16x32_bf16 v[30:33], v[154:157], v[204:207], v[30:33]
	v_mfma_f32_16x16x32_bf16 v[26:29], v[162:165], v[204:207], v[26:29]
	v_mfma_f32_16x16x32_bf16 v[14:17], v[154:157], v[212:215], v[14:17]
	v_mfma_f32_16x16x32_bf16 v[10:13], v[162:165], v[212:215], v[10:13]
	v_mfma_f32_16x16x32_bf16 v[54:57], v[166:169], v[182:185], v[54:57]
	v_mfma_f32_16x16x32_bf16 v[50:53], v[174:177], v[182:185], v[50:53]
	v_mfma_f32_16x16x32_bf16 v[38:41], v[166:169], v[190:193], v[38:41]
	v_mfma_f32_16x16x32_bf16 v[34:37], v[174:177], v[190:193], v[34:37]
	v_mfma_f32_16x16x32_bf16 v[22:25], v[166:169], v[198:201], v[22:25]
	v_mfma_f32_16x16x32_bf16 v[18:21], v[174:177], v[198:201], v[18:21]
	v_mfma_f32_16x16x32_bf16 v[6:9], v[166:169], v[208:211], v[6:9]
	v_mfma_f32_16x16x32_bf16 v[2:5], v[174:177], v[208:211], v[2:5]
	v_mfma_f32_16x16x32_bf16 v[54:57], v[170:173], v[186:189], v[54:57]
	v_mfma_f32_16x16x32_bf16 v[50:53], v[178:181], v[186:189], v[50:53]
	v_mfma_f32_16x16x32_bf16 v[38:41], v[170:173], v[194:197], v[38:41]
	v_mfma_f32_16x16x32_bf16 v[34:37], v[178:181], v[194:197], v[34:37]
	v_mfma_f32_16x16x32_bf16 v[22:25], v[170:173], v[204:207], v[22:25]
	v_mfma_f32_16x16x32_bf16 v[18:21], v[178:181], v[204:207], v[18:21]
	v_mfma_f32_16x16x32_bf16 v[6:9], v[170:173], v[212:215], v[6:9]
	v_mfma_f32_16x16x32_bf16 v[2:5], v[178:181], v[212:215], v[2:5]
	s_setprio 0
	s_barrier
	s_add_i32 s49, s49, 2
	s_add_u32 s50, s50, 0x100
	s_addc_u32 s51, s51, 0
	s_add_u32 s41, s41, 0x100
	s_addc_u32 s43, s43, 0
	s_cmp_gt_u32 s49, 29
	s_cbranch_scc0 .LBB0_571
	s_and_b64 vcc, exec, s[38:39]
	s_cbranch_vccz .LBB0_574
	s_barrier

; #define PG8_STAGE(bufoff, gbase, voff) do { _Pragma("unroll") for (int _i = 0; _i < 2; ++_i) \
;         __builtin_amdgcn_global_load_lds((const unsigned*)((const char*)(gbase) + (voff)[_i]), (PG8_LAS unsigned*)(lds + (bufoff) + ldsw + _i * 8192), 16, 0, 0); } while (0)
; #define PG8_LDA(dst, b, h) do { _Pragma("unroll") for (int m = 0; m < 4; ++m) _Pragma("unroll") for (int k = 0; k < 2; ++k) dst[m][k] = *(const PG8_LAS bf16x8*)(lds + PG8_SA(b, h) + aoff + m * 2048 + k * 1024); } while (0)
; #define PG8_LDB(dst, b, h) do { _Pragma("unroll") for (int n = 0; n < 2; ++n) _Pragma("unroll") for (int k = 0; k < 2; ++k) dst[n][k] = *(const PG8_LAS bf16x8*)(lds + PG8_SB(b, h) + boff + n * 2048 + k * 1024); } while (0)
; #define PG8_MMA(ai, bj, At, Bt) do { __builtin_amdgcn_s_setprio(1); _Pragma("unroll") for (int m = 0; m < 4; ++m) _Pragma("unroll") for (int n = 0; n < 2; ++n) _Pragma("unroll") for (int k = 0; k < 2; ++k) \
;         acc[ai][bj][m][n] = __builtin_amdgcn_mfma_f32_16x16x32_bf16(Bt[n][k], At[m][k], acc[ai][bj][m][n], 0, 0, 0); __builtin_amdgcn_s_setprio(0); } while (0)
; #define PG8_WAIT_V(n) asm volatile("s_waitcnt vmcnt(" #n ")" ::: "memory")
; #define PG8_WAIT_L(n) asm volatile("s_waitcnt lgkmcnt(" #n ")" ::: "memory")
; template <class Epi, class Sched, bool ALIGN_EPI = false, bool SP2 = false>
; __device__ __forceinline__ void gemm_phase(PG8_LAS unsigned char* lds, const Gemm g, const Sched& S, const Epi& E) {
;     ...
;             const bool last = (t == nt - 2);
;             const char* a1 = cA + (size_t)(t + 1) * kstep;
;             const char* a2 = last ? nA : cA + (size_t)(t + 2) * kstep; const char* b2 = last ? nB : cB + (size_t)(t + 2) * kstep;
;             const char* a3 = a2 + kstep; const char* b3 = b2 + kstep;
;             if (last && has_next) S.a_ready(nxt);
;             if constexpr (SP2) {
;             PG8_LDB(B0, 0, 0); PG8_LDB(B1, 0, 1); PG8_SCHED; PG8_LDA(At, 0, 0); PG8_STAGEA(PG8_SA(1, 1), a1, 1, false);
;             PG8_WAIT_V(8); PG8_WAIT_L(0); PG8_BAR; PG8_MMA(0, 0, At, B0); PG8_MMA(0, 1, At, B1); PG8_BAR; PG8_SCHED;
;             PG8_LDA(At, 0, 1); PG8_STAGE(PG8_SB(0, 0), b2, voffB); PG8_STAGE(PG8_SB(0, 1), b2 + hstep, voffB); PG8_STAGEA(PG8_SA(0, 0), a2, 0, last);
;             PG8_WAIT_V(8); PG8_WAIT_L(0); PG8_BAR; PG8_MMA(1, 0, At, B0); PG8_MMA(1, 1, At, B1); PG8_BAR; PG8_SCHED;
.LBB0_792:
	s_add_u32 s6, s12, 0x100
	v_add_u32_e32 v134, s84, v152
	s_addc_u32 s7, s13, 0
	ds_read_b128 v[162:165], v134
	ds_read_b128 v[166:169], v134 offset:1024
	ds_read_b128 v[170:173], v134 offset:2048
	ds_read_b128 v[174:177], v134 offset:3072
	v_add_u32_e32 v134, s85, v152
	s_add_u32 s10, s16, s12
	ds_read_b128 v[178:181], v134
	ds_read_b128 v[182:185], v134 offset:1024
	ds_read_b128 v[186:189], v134 offset:2048
	ds_read_b128 v[190:193], v134 offset:3072
	s_addc_u32 s11, s17, s13
	s_cmpk_eq_i32 s12, 0xf00
	s_cselect_b64 vcc, -1, 0
	s_and_b64 s[8:9], vcc, exec
	s_cselect_b32 s36, 0, s6
	s_cselect_b32 s27, 0, s7
	s_cselect_b32 s8, s18, s10
	s_cselect_b32 s9, s15, s11
	s_add_u32 s10, s42, s36
	s_addc_u32 s11, s43, s27
	v_lshl_add_u64 v[228:229], v[142:143], 0, s[12:13]
	s_add_i32 m0, s77, 0xc000
	ds_read_b128 v[194:197], v156
	ds_read_b128 v[198:201], v156 offset:1024
	ds_read_b128 v[204:207], v156 offset:2048
	ds_read_b128 v[208:211], v156 offset:3072
	ds_read_b128 v[212:215], v156 offset:4096
	ds_read_b128 v[216:219], v156 offset:5120
	ds_read_b128 v[220:223], v156 offset:6144
	ds_read_b128 v[224:227], v156 offset:7168
	global_load_lds_dwordx4 v[228:229], off
	v_lshl_add_u64 v[228:229], v[144:145], 0, s[12:13]
	s_add_i32 m0, s77, 0xe000
	s_nop 0
	global_load_lds_dwordx4 v[228:229], off
	s_waitcnt vmcnt(8) lgkmcnt(0)
	s_barrier
	s_setprio 1
	v_mfma_f32_16x16x32_bf16 v[126:129], v[162:165], v[194:197], v[126:129]
	v_mfma_f32_16x16x32_bf16 v[118:121], v[170:173], v[194:197], v[118:121]
	v_mfma_f32_16x16x32_bf16 v[110:113], v[162:165], v[204:207], v[110:113]
	v_mfma_f32_16x16x32_bf16 v[102:105], v[170:173], v[204:207], v[102:105]
	v_mfma_f32_16x16x32_bf16 v[94:97], v[162:165], v[212:215], v[94:97]
	v_mfma_f32_16x16x32_bf16 v[86:89], v[170:173], v[212:215], v[86:89]
	v_mfma_f32_16x16x32_bf16 v[78:81], v[162:165], v[220:223], v[78:81]
	v_mfma_f32_16x16x32_bf16 v[70:73], v[170:173], v[220:223], v[70:73]
	v_mfma_f32_16x16x32_bf16 v[126:129], v[166:169], v[198:201], v[126:129]
	v_mfma_f32_16x16x32_bf16 v[118:121], v[174:177], v[198:201], v[118:121]
	v_mfma_f32_16x16x32_bf16 v[110:113], v[166:169], v[208:211], v[110:113]
	v_mfma_f32_16x16x32_bf16 v[102:105], v[174:177], v[208:211], v[102:105]
	v_mfma_f32_16x16x32_bf16 v[94:97], v[166:169], v[216:219], v[94:97]
	v_mfma_f32_16x16x32_bf16 v[86:89], v[174:177], v[216:219], v[86:89]
	v_mfma_f32_16x16x32_bf16 v[78:81], v[166:169], v[224:227], v[78:81]
	v_mfma_f32_16x16x32_bf16 v[70:73], v[174:177], v[224:227], v[70:73]
	v_mfma_f32_16x16x32_bf16 v[122:125], v[178:181], v[194:197], v[122:125]
	v_mfma_f32_16x16x32_bf16 v[114:117], v[186:189], v[194:197], v[114:117]
	v_mfma_f32_16x16x32_bf16 v[106:109], v[178:181], v[204:207], v[106:109]
	v_mfma_f32_16x16x32_bf16 v[98:101], v[186:189], v[204:207], v[98:101]
	v_mfma_f32_16x16x32_bf16 v[90:93], v[178:181], v[212:215], v[90:93]
	v_mfma_f32_16x16x32_bf16 v[82:85], v[186:189], v[212:215], v[82:85]
	v_mfma_f32_16x16x32_bf16 v[74:77], v[178:181], v[220:223], v[74:77]
	v_mfma_f32_16x16x32_bf16 v[66:69], v[186:189], v[220:223], v[66:69]
	v_mfma_f32_16x16x32_bf16 v[122:125], v[182:185], v[198:201], v[122:125]
	v_mfma_f32_16x16x32_bf16 v[114:117], v[190:193], v[198:201], v[114:117]
	v_mfma_f32_16x16x32_bf16 v[106:109], v[182:185], v[208:211], v[106:109]
	v_mfma_f32_16x16x32_bf16 v[98:101], v[190:193], v[208:211], v[98:101]
	v_mfma_f32_16x16x32_bf16 v[90:93], v[182:185], v[216:219], v[90:93]
	v_mfma_f32_16x16x32_bf16 v[82:85], v[190:193], v[216:219], v[82:85]
	v_mfma_f32_16x16x32_bf16 v[74:77], v[182:185], v[224:227], v[74:77]
	v_mfma_f32_16x16x32_bf16 v[66:69], v[190:193], v[224:227], v[66:69]
	s_setprio 0
	s_barrier
	s_add_i32 s12, s84, s76
	v_lshl_add_u64 v[228:229], s[8:9], 0, v[130:131]
	s_mov_b32 m0, s12
	ds_read_b128 v[194:197], v156 offset:16384
	ds_read_b128 v[198:201], v156 offset:17408
	ds_read_b128 v[204:207], v156 offset:18432
	ds_read_b128 v[208:211], v156 offset:19456
	ds_read_b128 v[212:215], v156 offset:20480
	ds_read_b128 v[216:219], v156 offset:21504
	ds_read_b128 v[220:223], v156 offset:22528
	ds_read_b128 v[224:227], v156 offset:23552
	global_load_lds_dwordx4 v[228:229], off
	s_add_i32 m0, s12, 0x2000
	s_add_u32 s12, s8, 0x80000
	v_lshl_add_u64 v[230:231], s[8:9], 0, v[132:133]
	s_addc_u32 s13, s9, 0
	s_add_i32 s27, s85, s76
	global_load_lds_dwordx4 v[230:231], off
	v_lshl_add_u64 v[232:233], s[12:13], 0, v[130:131]
	s_mov_b32 m0, s27
	v_cndmask_b32_e32 v134, v146, v157, vcc
	global_load_lds_dwordx4 v[232:233], off
	v_lshl_add_u64 v[232:233], s[12:13], 0, v[132:133]
	s_add_i32 m0, s27, 0x2000
	s_nop 0
	global_load_lds_dwordx4 v[232:233], off
	s_mov_b32 m0, s77
	v_lshl_add_u64 v[232:233], s[10:11], 0, v[134:135]
	global_load_lds_dwordx4 v134, s[10:11]
	v_cndmask_b32_e32 v134, v136, v158, vcc
	s_mov_b32 m0, s78
	v_lshl_add_u64 v[234:235], s[10:11], 0, v[134:135]
	global_load_lds_dwordx4 v134, s[10:11]
	s_waitcnt vmcnt(8) lgkmcnt(0)
	s_barrier
; #define PG8_LDA(dst, b, h) do { _Pragma("unroll") for (int m = 0; m < 4; ++m) _Pragma("unroll") for (int k = 0; k < 2; ++k) dst[m][k] = *(const PG8_LAS bf16x8*)(lds + PG8_SA(b, h) + aoff + m * 2048 + k * 1024); } while (0)
; #define PG8_LDB(dst, b, h) do { _Pragma("unroll") for (int n = 0; n < 2; ++n) _Pragma("unroll") for (int k = 0; k < 2; ++k) dst[n][k] = *(const PG8_LAS bf16x8*)(lds + PG8_SB(b, h) + boff + n * 2048 + k * 1024); } while (0)
; #define PG8_MMA(ai, bj, At, Bt) do { __builtin_amdgcn_s_setprio(1); _Pragma("unroll") for (int m = 0; m < 4; ++m) _Pragma("unroll") for (int n = 0; n < 2; ++n) _Pragma("unroll") for (int k = 0; k < 2; ++k) \
;         acc[ai][bj][m][n] = __builtin_amdgcn_mfma_f32_16x16x32_bf16(Bt[n][k], At[m][k], acc[ai][bj][m][n], 0, 0, 0); __builtin_amdgcn_s_setprio(0); } while (0)
; #define PG8_WAIT_V(n) asm volatile("s_waitcnt vmcnt(" #n ")" ::: "memory")
; #define PG8_WAIT_L(n) asm volatile("s_waitcnt lgkmcnt(" #n ")" ::: "memory")
; #define PG8_BAR __builtin_amdgcn_s_barrier()
; #define PG8_SCHED __builtin_amdgcn_sched_barrier(0)
; template <class Epi, class Sched, bool ALIGN_EPI = false, bool SP2 = false>
; __device__ __forceinline__ void gemm_phase(PG8_LAS unsigned char* lds, const Gemm g, const Sched& S, const Epi& E) {
;     ...
;             PG8_WAIT_V(8); PG8_WAIT_L(0); PG8_BAR; PG8_MMA(1, 0, At, B0); PG8_MMA(1, 1, At, B1); PG8_BAR; PG8_SCHED;
;             PG8_LDB(B0, 1, 0); PG8_LDB(B1, 1, 1); PG8_SCHED; PG8_LDA(At, 1, 0); PG8_STAGEA(PG8_SA(0, 1), a2, 1, last);
;             PG8_WAIT_V(8); PG8_WAIT_L(0); PG8_BAR; PG8_MMA(0, 0, At, B0); PG8_MMA(0, 1, At, B1); PG8_BAR; PG8_SCHED;
	s_setprio 1
	v_mfma_f32_16x16x32_bf16 v[62:65], v[162:165], v[194:197], v[62:65]
	v_mfma_f32_16x16x32_bf16 v[54:57], v[170:173], v[194:197], v[54:57]
	v_mfma_f32_16x16x32_bf16 v[46:49], v[162:165], v[204:207], v[46:49]
	v_mfma_f32_16x16x32_bf16 v[38:41], v[170:173], v[204:207], v[38:41]
	v_mfma_f32_16x16x32_bf16 v[30:33], v[162:165], v[212:215], v[30:33]
	v_mfma_f32_16x16x32_bf16 v[22:25], v[170:173], v[212:215], v[22:25]
	v_mfma_f32_16x16x32_bf16 v[14:17], v[162:165], v[220:223], v[14:17]
	v_mfma_f32_16x16x32_bf16 v[6:9], v[170:173], v[220:223], v[6:9]
	v_mfma_f32_16x16x32_bf16 v[62:65], v[166:169], v[198:201], v[62:65]
	v_mfma_f32_16x16x32_bf16 v[54:57], v[174:177], v[198:201], v[54:57]
	v_mfma_f32_16x16x32_bf16 v[46:49], v[166:169], v[208:211], v[46:49]
	v_mfma_f32_16x16x32_bf16 v[38:41], v[174:177], v[208:211], v[38:41]
	v_mfma_f32_16x16x32_bf16 v[30:33], v[166:169], v[216:219], v[30:33]
	v_mfma_f32_16x16x32_bf16 v[22:25], v[174:177], v[216:219], v[22:25]
	v_mfma_f32_16x16x32_bf16 v[14:17], v[166:169], v[224:227], v[14:17]
	v_mfma_f32_16x16x32_bf16 v[6:9], v[174:177], v[224:227], v[6:9]
	v_mfma_f32_16x16x32_bf16 v[58:61], v[178:181], v[194:197], v[58:61]
	v_mfma_f32_16x16x32_bf16 v[50:53], v[186:189], v[194:197], v[50:53]
	v_mfma_f32_16x16x32_bf16 v[42:45], v[178:181], v[204:207], v[42:45]
	v_mfma_f32_16x16x32_bf16 v[34:37], v[186:189], v[204:207], v[34:37]
	v_mfma_f32_16x16x32_bf16 v[26:29], v[178:181], v[212:215], v[26:29]
	v_mfma_f32_16x16x32_bf16 v[18:21], v[186:189], v[212:215], v[18:21]
	v_mfma_f32_16x16x32_bf16 v[10:13], v[178:181], v[220:223], v[10:13]
	v_mfma_f32_16x16x32_bf16 v[2:5], v[186:189], v[220:223], v[2:5]
	v_mfma_f32_16x16x32_bf16 v[58:61], v[182:185], v[198:201], v[58:61]
	v_mfma_f32_16x16x32_bf16 v[50:53], v[190:193], v[198:201], v[50:53]
	v_mfma_f32_16x16x32_bf16 v[42:45], v[182:185], v[208:211], v[42:45]
	v_mfma_f32_16x16x32_bf16 v[34:37], v[190:193], v[208:211], v[34:37]
	v_mfma_f32_16x16x32_bf16 v[26:29], v[182:185], v[216:219], v[26:29]
	v_mfma_f32_16x16x32_bf16 v[18:21], v[190:193], v[216:219], v[18:21]
	v_mfma_f32_16x16x32_bf16 v[10:13], v[182:185], v[224:227], v[10:13]
	v_mfma_f32_16x16x32_bf16 v[2:5], v[190:193], v[224:227], v[2:5]
	s_setprio 0
	s_barrier
	s_add_i32 s12, 0, 0x18000
	v_add_u32_e32 v134, s12, v152
	s_add_i32 s13, 0, 0x1c000
	ds_read_b128 v[162:165], v134
	ds_read_b128 v[166:169], v134 offset:1024
	ds_read_b128 v[170:173], v134 offset:2048
	ds_read_b128 v[174:177], v134 offset:3072
	v_add_u32_e32 v134, s13, v152
	ds_read_b128 v[178:181], v134
	ds_read_b128 v[182:185], v134 offset:1024
	ds_read_b128 v[186:189], v134 offset:2048
	ds_read_b128 v[190:193], v134 offset:3072
	s_mov_b32 m0, s79
	v_cndmask_b32_e32 v134, v138, v159, vcc
	ds_read_b128 v[194:197], v156 offset:32768
	ds_read_b128 v[198:201], v156 offset:33792
	ds_read_b128 v[204:207], v156 offset:34816
	ds_read_b128 v[208:211], v156 offset:35840
	ds_read_b128 v[212:215], v156 offset:36864
	ds_read_b128 v[216:219], v156 offset:37888
	ds_read_b128 v[220:223], v156 offset:38912
	ds_read_b128 v[224:227], v156 offset:39936
	global_load_lds_dwordx4 v134, s[10:11]
	v_cndmask_b32_e32 v134, v140, v160, vcc
	s_mov_b32 m0, s80
	s_nop 0
	global_load_lds_dwordx4 v134, s[10:11]
	s_waitcnt vmcnt(8) lgkmcnt(0)
	s_barrier
	s_setprio 1
	v_mfma_f32_16x16x32_bf16 v[126:129], v[162:165], v[194:197], v[126:129]
	v_mfma_f32_16x16x32_bf16 v[118:121], v[170:173], v[194:197], v[118:121]
	v_mfma_f32_16x16x32_bf16 v[110:113], v[162:165], v[204:207], v[110:113]
	v_mfma_f32_16x16x32_bf16 v[102:105], v[170:173], v[204:207], v[102:105]
	v_mfma_f32_16x16x32_bf16 v[94:97], v[162:165], v[212:215], v[94:97]
	v_mfma_f32_16x16x32_bf16 v[86:89], v[170:173], v[212:215], v[86:89]
	v_mfma_f32_16x16x32_bf16 v[78:81], v[162:165], v[220:223], v[78:81]
	v_mfma_f32_16x16x32_bf16 v[70:73], v[170:173], v[220:223], v[70:73]
	v_mfma_f32_16x16x32_bf16 v[126:129], v[166:169], v[198:201], v[126:129]
	v_mfma_f32_16x16x32_bf16 v[118:121], v[174:177], v[198:201], v[118:121]
	v_mfma_f32_16x16x32_bf16 v[110:113], v[166:169], v[208:211], v[110:113]
	v_mfma_f32_16x16x32_bf16 v[102:105], v[174:177], v[208:211], v[102:105]
	v_mfma_f32_16x16x32_bf16 v[94:97], v[166:169], v[216:219], v[94:97]
	v_mfma_f32_16x16x32_bf16 v[86:89], v[174:177], v[216:219], v[86:89]
	v_mfma_f32_16x16x32_bf16 v[78:81], v[166:169], v[224:227], v[78:81]
	v_mfma_f32_16x16x32_bf16 v[70:73], v[174:177], v[224:227], v[70:73]
	v_mfma_f32_16x16x32_bf16 v[122:125], v[178:181], v[194:197], v[122:125]
	v_mfma_f32_16x16x32_bf16 v[114:117], v[186:189], v[194:197], v[114:117]
	v_mfma_f32_16x16x32_bf16 v[106:109], v[178:181], v[204:207], v[106:109]
	v_mfma_f32_16x16x32_bf16 v[98:101], v[186:189], v[204:207], v[98:101]
	v_mfma_f32_16x16x32_bf16 v[90:93], v[178:181], v[212:215], v[90:93]
	v_mfma_f32_16x16x32_bf16 v[82:85], v[186:189], v[212:215], v[82:85]
	v_mfma_f32_16x16x32_bf16 v[74:77], v[178:181], v[220:223], v[74:77]
	v_mfma_f32_16x16x32_bf16 v[66:69], v[186:189], v[220:223], v[66:69]
	v_mfma_f32_16x16x32_bf16 v[122:125], v[182:185], v[198:201], v[122:125]
	v_mfma_f32_16x16x32_bf16 v[114:117], v[190:193], v[198:201], v[114:117]
	v_mfma_f32_16x16x32_bf16 v[106:109], v[182:185], v[208:211], v[106:109]
	v_mfma_f32_16x16x32_bf16 v[98:101], v[190:193], v[208:211], v[98:101]
	v_mfma_f32_16x16x32_bf16 v[90:93], v[182:185], v[216:219], v[90:93]
	v_mfma_f32_16x16x32_bf16 v[82:85], v[190:193], v[216:219], v[82:85]
	v_mfma_f32_16x16x32_bf16 v[74:77], v[182:185], v[224:227], v[74:77]
	v_mfma_f32_16x16x32_bf16 v[66:69], v[190:193], v[224:227], v[66:69]
	s_setprio 0
	s_barrier
; #define PG8_STAGE(bufoff, gbase, voff) do { _Pragma("unroll") for (int _i = 0; _i < 2; ++_i) \
;         __builtin_amdgcn_global_load_lds((const unsigned*)((const char*)(gbase) + (voff)[_i]), (PG8_LAS unsigned*)(lds + (bufoff) + ldsw + _i * 8192), 16, 0, 0); } while (0)
; #define PG8_LDA(dst, b, h) do { _Pragma("unroll") for (int m = 0; m < 4; ++m) _Pragma("unroll") for (int k = 0; k < 2; ++k) dst[m][k] = *(const PG8_LAS bf16x8*)(lds + PG8_SA(b, h) + aoff + m * 2048 + k * 1024); } while (0)
; #define PG8_MMA(ai, bj, At, Bt) do { __builtin_amdgcn_s_setprio(1); _Pragma("unroll") for (int m = 0; m < 4; ++m) _Pragma("unroll") for (int n = 0; n < 2; ++n) _Pragma("unroll") for (int k = 0; k < 2; ++k) \
;         acc[ai][bj][m][n] = __builtin_amdgcn_mfma_f32_16x16x32_bf16(Bt[n][k], At[m][k], acc[ai][bj][m][n], 0, 0, 0); __builtin_amdgcn_s_setprio(0); } while (0)
; #define PG8_WAIT_V(n) asm volatile("s_waitcnt vmcnt(" #n ")" ::: "memory")
; #define PG8_WAIT_L(n) asm volatile("s_waitcnt lgkmcnt(" #n ")" ::: "memory")
; #define PG8_BAR __builtin_amdgcn_s_barrier()
; #define PG8_SCHED __builtin_amdgcn_sched_barrier(0)
; template <class Epi, class Sched, bool ALIGN_EPI = false, bool SP2 = false>
; __device__ __forceinline__ void gemm_phase(PG8_LAS unsigned char* lds, const Gemm g, const Sched& S, const Epi& E) {
;     ...
;             PG8_LDA(At, 1, 1); PG8_STAGE(PG8_SB(1, 0), b3, voffB); PG8_STAGE(PG8_SB(1, 1), b3 + hstep, voffB); PG8_STAGEA(PG8_SA(1, 0), a3, 0, last);
;             PG8_WAIT_V(8); PG8_WAIT_L(0); PG8_BAR; PG8_MMA(1, 0, At, B0); PG8_MMA(1, 1, At, B1); PG8_BAR; PG8_SCHED;
	s_add_i32 s10, s12, s76
	v_lshl_add_u64 v[228:229], v[228:229], 0, s[52:53]
	s_mov_b32 m0, s10
	ds_read_b128 v[194:197], v156 offset:49152
	ds_read_b128 v[198:201], v156 offset:50176
	ds_read_b128 v[204:207], v156 offset:51200
	ds_read_b128 v[208:211], v156 offset:52224
	ds_read_b128 v[212:215], v156 offset:53248
	ds_read_b128 v[216:219], v156 offset:54272
	ds_read_b128 v[220:223], v156 offset:55296
	ds_read_b128 v[224:227], v156 offset:56320
	global_load_lds_dwordx4 v[228:229], off
	s_add_i32 m0, s10, 0x2000
	s_add_u32 s8, s8, 0x80080
	v_lshl_add_u64 v[228:229], v[230:231], 0, s[52:53]
	s_addc_u32 s9, s9, 0
	s_add_i32 s10, s13, s76
	global_load_lds_dwordx4 v[228:229], off
	v_lshl_add_u64 v[228:229], s[8:9], 0, v[130:131]
	s_mov_b32 m0, s10
	s_nop 0
	global_load_lds_dwordx4 v[228:229], off
	v_lshl_add_u64 v[228:229], s[8:9], 0, v[132:133]
	s_add_i32 m0, s10, 0x2000
	s_nop 0
	global_load_lds_dwordx4 v[228:229], off
	v_lshl_add_u64 v[228:229], v[232:233], 0, s[52:53]
	s_mov_b32 m0, s81
	s_nop 0
	global_load_lds_dwordx4 v[228:229], off
	v_lshl_add_u64 v[228:229], v[234:235], 0, s[52:53]
	s_mov_b32 m0, s82
	s_nop 0
	global_load_lds_dwordx4 v[228:229], off
	s_waitcnt vmcnt(8) lgkmcnt(0)
	s_barrier
	s_setprio 1
	v_mfma_f32_16x16x32_bf16 v[62:65], v[162:165], v[194:197], v[62:65]
	v_mfma_f32_16x16x32_bf16 v[54:57], v[170:173], v[194:197], v[54:57]
	v_mfma_f32_16x16x32_bf16 v[46:49], v[162:165], v[204:207], v[46:49]
	v_mfma_f32_16x16x32_bf16 v[38:41], v[170:173], v[204:207], v[38:41]
	v_mfma_f32_16x16x32_bf16 v[30:33], v[162:165], v[212:215], v[30:33]
	v_mfma_f32_16x16x32_bf16 v[22:25], v[170:173], v[212:215], v[22:25]
	v_mfma_f32_16x16x32_bf16 v[14:17], v[162:165], v[220:223], v[14:17]
	v_mfma_f32_16x16x32_bf16 v[6:9], v[170:173], v[220:223], v[6:9]
	v_mfma_f32_16x16x32_bf16 v[62:65], v[166:169], v[198:201], v[62:65]
	v_mfma_f32_16x16x32_bf16 v[54:57], v[174:177], v[198:201], v[54:57]
	v_mfma_f32_16x16x32_bf16 v[46:49], v[166:169], v[208:211], v[46:49]
	v_mfma_f32_16x16x32_bf16 v[38:41], v[174:177], v[208:211], v[38:41]
	v_mfma_f32_16x16x32_bf16 v[30:33], v[166:169], v[216:219], v[30:33]
	v_mfma_f32_16x16x32_bf16 v[22:25], v[174:177], v[216:219], v[22:25]
	v_mfma_f32_16x16x32_bf16 v[14:17], v[166:169], v[224:227], v[14:17]
	v_mfma_f32_16x16x32_bf16 v[6:9], v[174:177], v[224:227], v[6:9]
	v_mfma_f32_16x16x32_bf16 v[58:61], v[178:181], v[194:197], v[58:61]
	v_mfma_f32_16x16x32_bf16 v[50:53], v[186:189], v[194:197], v[50:53]
	v_mfma_f32_16x16x32_bf16 v[42:45], v[178:181], v[204:207], v[42:45]
	v_mfma_f32_16x16x32_bf16 v[34:37], v[186:189], v[204:207], v[34:37]
	v_mfma_f32_16x16x32_bf16 v[26:29], v[178:181], v[212:215], v[26:29]
	v_mfma_f32_16x16x32_bf16 v[18:21], v[186:189], v[212:215], v[18:21]
	v_mfma_f32_16x16x32_bf16 v[10:13], v[178:181], v[220:223], v[10:13]
	v_mfma_f32_16x16x32_bf16 v[2:5], v[186:189], v[220:223], v[2:5]
	v_mfma_f32_16x16x32_bf16 v[58:61], v[182:185], v[198:201], v[58:61]
	v_mfma_f32_16x16x32_bf16 v[50:53], v[190:193], v[198:201], v[50:53]
	v_mfma_f32_16x16x32_bf16 v[42:45], v[182:185], v[208:211], v[42:45]
	v_mfma_f32_16x16x32_bf16 v[34:37], v[190:193], v[208:211], v[34:37]
	v_mfma_f32_16x16x32_bf16 v[26:29], v[182:185], v[216:219], v[26:29]
	v_mfma_f32_16x16x32_bf16 v[18:21], v[190:193], v[216:219], v[18:21]
	v_mfma_f32_16x16x32_bf16 v[10:13], v[182:185], v[224:227], v[10:13]
	v_mfma_f32_16x16x32_bf16 v[2:5], v[190:193], v[224:227], v[2:5]
	s_setprio 0
	s_barrier
	s_add_i32 s19, s19, 2
	s_cmp_gt_u32 s19, 29
	s_mov_b64 s[12:13], s[6:7]
	s_cbranch_scc0 .LBB0_792
	s_and_b64 vcc, exec, s[56:57]
	s_cbranch_vccz .LBB0_795
	s_barrier

; #define PG8_STAGE(bufoff, gbase, voff) do { _Pragma("unroll") for (int _i = 0; _i < 2; ++_i) \
;         __builtin_amdgcn_global_load_lds((const unsigned*)((const char*)(gbase) + (voff)[_i]), (PG8_LAS unsigned*)(lds + (bufoff) + ldsw + _i * 8192), 16, 0, 0); } while (0)
; #define PG8_LDA(dst, b, h) do { _Pragma("unroll") for (int m = 0; m < 4; ++m) _Pragma("unroll") for (int k = 0; k < 2; ++k) dst[m][k] = *(const PG8_LAS bf16x8*)(lds + PG8_SA(b, h) + aoff + m * 2048 + k * 1024); } while (0)
; #define PG8_LDB(dst, b, h) do { _Pragma("unroll") for (int n = 0; n < 2; ++n) _Pragma("unroll") for (int k = 0; k < 2; ++k) dst[n][k] = *(const PG8_LAS bf16x8*)(lds + PG8_SB(b, h) + boff + n * 2048 + k * 1024); } while (0)
; #define PG8_MMA(ai, bj, At, Bt) do { __builtin_amdgcn_s_setprio(1); _Pragma("unroll") for (int m = 0; m < 4; ++m) _Pragma("unroll") for (int n = 0; n < 2; ++n) _Pragma("unroll") for (int k = 0; k < 2; ++k) \
;         acc[ai][bj][m][n] = __builtin_amdgcn_mfma_f32_16x16x32_bf16(Bt[n][k], At[m][k], acc[ai][bj][m][n], 0, 0, 0); __builtin_amdgcn_s_setprio(0); } while (0)
; #define PG8_WAIT_V(n) asm volatile("s_waitcnt vmcnt(" #n ")" ::: "memory")
; #define PG8_WAIT_L(n) asm volatile("s_waitcnt lgkmcnt(" #n ")" ::: "memory")
; template <class Epi, class Sched, bool ALIGN_EPI = false, bool SP2 = false>
; __device__ __forceinline__ void gemm_phase(PG8_LAS unsigned char* lds, const Gemm g, const Sched& S, const Epi& E) {
;     ...
;             const bool last = (t == nt - 2);
;             const char* a1 = cA + (size_t)(t + 1) * kstep;
;             const char* a2 = last ? nA : cA + (size_t)(t + 2) * kstep; const char* b2 = last ? nB : cB + (size_t)(t + 2) * kstep;
;             const char* a3 = a2 + kstep; const char* b3 = b2 + kstep;
;             if (last && has_next) S.a_ready(nxt);
;             if constexpr (SP2) {
;             PG8_LDB(B0, 0, 0); PG8_LDB(B1, 0, 1); PG8_SCHED; PG8_LDA(At, 0, 0); PG8_STAGEA(PG8_SA(1, 1), a1, 1, false);
;             PG8_WAIT_V(8); PG8_WAIT_L(0); PG8_BAR; PG8_MMA(0, 0, At, B0); PG8_MMA(0, 1, At, B1); PG8_BAR; PG8_SCHED;
;             PG8_LDA(At, 0, 1); PG8_STAGE(PG8_SB(0, 0), b2, voffB); PG8_STAGE(PG8_SB(0, 1), b2 + hstep, voffB); PG8_STAGEA(PG8_SA(0, 0), a2, 0, last);
;             PG8_WAIT_V(8); PG8_WAIT_L(0); PG8_BAR; PG8_MMA(1, 0, At, B0); PG8_MMA(1, 1, At, B1); PG8_BAR; PG8_SCHED;
.LBB0_927:
	v_add_u32_e32 v147, s76, v142
	ds_read_b128 v[148:151], v147
	ds_read_b128 v[152:155], v147 offset:1024
	ds_read_b128 v[156:159], v147 offset:2048
	ds_read_b128 v[160:163], v147 offset:3072
	v_add_u32_e32 v147, s77, v142
	ds_read_b128 v[164:167], v147
	ds_read_b128 v[168:171], v147 offset:1024
	ds_read_b128 v[172:175], v147 offset:2048
	ds_read_b128 v[176:179], v147 offset:3072
	s_add_u32 s60, s58, 0xfffe0080
	s_addc_u32 s61, s59, -1
	s_cmp_eq_u32 s83, 4
	s_cselect_b32 s63, s9, s61
	s_cselect_b32 s62, s11, s60
	s_cselect_b32 s61, s36, s49
	s_cselect_b32 s60, s37, s47
	v_lshl_add_u64 v[200:201], s[58:59], 0, v[138:139]
	s_add_i32 m0, s57, 0xc000
	ds_read_b128 v[180:183], v146
	ds_read_b128 v[184:187], v146 offset:1024
	ds_read_b128 v[188:191], v146 offset:2048
	ds_read_b128 v[192:195], v146 offset:3072
	ds_read_b128 v[196:199], v146 offset:4096
	ds_read_b128 v[204:207], v146 offset:5120
	ds_read_b128 v[208:211], v146 offset:6144
	ds_read_b128 v[212:215], v146 offset:7168
	global_load_lds_dwordx4 v[200:201], off
	v_lshl_add_u64 v[200:201], s[58:59], 0, v[140:141]
	s_add_i32 m0, s57, 0xe000
	s_nop 0
	global_load_lds_dwordx4 v[200:201], off
	s_waitcnt vmcnt(8) lgkmcnt(0)
	s_barrier
	s_setprio 1
	v_mfma_f32_16x16x32_bf16 v[122:125], v[148:151], v[180:183], v[122:125]
	v_mfma_f32_16x16x32_bf16 v[126:129], v[156:159], v[180:183], v[126:129]
	v_mfma_f32_16x16x32_bf16 v[106:109], v[148:151], v[188:191], v[106:109]
	v_mfma_f32_16x16x32_bf16 v[110:113], v[156:159], v[188:191], v[110:113]
	v_mfma_f32_16x16x32_bf16 v[90:93], v[148:151], v[196:199], v[90:93]
	v_mfma_f32_16x16x32_bf16 v[94:97], v[156:159], v[196:199], v[94:97]
	v_mfma_f32_16x16x32_bf16 v[74:77], v[148:151], v[208:211], v[74:77]
	v_mfma_f32_16x16x32_bf16 v[78:81], v[156:159], v[208:211], v[78:81]
	v_mfma_f32_16x16x32_bf16 v[122:125], v[152:155], v[184:187], v[122:125]
	v_mfma_f32_16x16x32_bf16 v[126:129], v[160:163], v[184:187], v[126:129]
	v_mfma_f32_16x16x32_bf16 v[106:109], v[152:155], v[192:195], v[106:109]
	v_mfma_f32_16x16x32_bf16 v[110:113], v[160:163], v[192:195], v[110:113]
	v_mfma_f32_16x16x32_bf16 v[90:93], v[152:155], v[204:207], v[90:93]
	v_mfma_f32_16x16x32_bf16 v[94:97], v[160:163], v[204:207], v[94:97]
	v_mfma_f32_16x16x32_bf16 v[74:77], v[152:155], v[212:215], v[74:77]
	v_mfma_f32_16x16x32_bf16 v[78:81], v[160:163], v[212:215], v[78:81]
	v_mfma_f32_16x16x32_bf16 v[114:117], v[164:167], v[180:183], v[114:117]
	v_mfma_f32_16x16x32_bf16 v[118:121], v[172:175], v[180:183], v[118:121]
	v_mfma_f32_16x16x32_bf16 v[98:101], v[164:167], v[188:191], v[98:101]
	v_mfma_f32_16x16x32_bf16 v[102:105], v[172:175], v[188:191], v[102:105]
	v_mfma_f32_16x16x32_bf16 v[82:85], v[164:167], v[196:199], v[82:85]
	v_mfma_f32_16x16x32_bf16 v[86:89], v[172:175], v[196:199], v[86:89]
	v_mfma_f32_16x16x32_bf16 v[66:69], v[164:167], v[208:211], v[66:69]
	v_mfma_f32_16x16x32_bf16 v[70:73], v[172:175], v[208:211], v[70:73]
	v_mfma_f32_16x16x32_bf16 v[114:117], v[168:171], v[184:187], v[114:117]
	v_mfma_f32_16x16x32_bf16 v[118:121], v[176:179], v[184:187], v[118:121]
	v_mfma_f32_16x16x32_bf16 v[98:101], v[168:171], v[192:195], v[98:101]
	v_mfma_f32_16x16x32_bf16 v[102:105], v[176:179], v[192:195], v[102:105]
	v_mfma_f32_16x16x32_bf16 v[82:85], v[168:171], v[204:207], v[82:85]
	v_mfma_f32_16x16x32_bf16 v[86:89], v[176:179], v[204:207], v[86:89]
	v_mfma_f32_16x16x32_bf16 v[66:69], v[168:171], v[212:215], v[66:69]
	v_mfma_f32_16x16x32_bf16 v[70:73], v[176:179], v[212:215], v[70:73]
	s_setprio 0
	s_barrier
	s_add_i32 s84, s76, s65
	v_lshl_add_u64 v[200:201], s[60:61], 0, v[132:133]
	s_mov_b32 m0, s84
	ds_read_b128 v[180:183], v146 offset:16384
	ds_read_b128 v[184:187], v146 offset:17408
	ds_read_b128 v[188:191], v146 offset:18432
	ds_read_b128 v[192:195], v146 offset:19456
	ds_read_b128 v[196:199], v146 offset:20480
	ds_read_b128 v[204:207], v146 offset:21504
	ds_read_b128 v[208:211], v146 offset:22528
	ds_read_b128 v[212:215], v146 offset:23552
	global_load_lds_dwordx4 v[200:201], off
	s_add_i32 m0, s84, 0x2000
	s_add_u32 s84, s60, 0x20000
	v_lshl_add_u64 v[216:217], s[60:61], 0, v[136:137]
	s_addc_u32 s85, s61, 0
	s_add_i32 s86, s77, s65
	global_load_lds_dwordx4 v[216:217], off
	v_lshl_add_u64 v[218:219], s[84:85], 0, v[132:133]
	s_mov_b32 m0, s86
	v_lshl_add_u64 v[220:221], s[62:63], 0, v[134:135]
	global_load_lds_dwordx4 v[218:219], off
	v_lshl_add_u64 v[218:219], s[84:85], 0, v[136:137]
	s_add_i32 m0, s86, 0x2000
	s_nop 0
	global_load_lds_dwordx4 v[218:219], off
	v_lshl_add_u64 v[218:219], s[62:63], 0, v[130:131]
	s_mov_b32 m0, s57
	s_nop 0
	global_load_lds_dwordx4 v[218:219], off
	s_mov_b32 m0, s66
	s_nop 0
	global_load_lds_dwordx4 v[220:221], off
	s_waitcnt vmcnt(8) lgkmcnt(0)
	s_barrier
; #define PG8_LDA(dst, b, h) do { _Pragma("unroll") for (int m = 0; m < 4; ++m) _Pragma("unroll") for (int k = 0; k < 2; ++k) dst[m][k] = *(const PG8_LAS bf16x8*)(lds + PG8_SA(b, h) + aoff + m * 2048 + k * 1024); } while (0)
; #define PG8_LDB(dst, b, h) do { _Pragma("unroll") for (int n = 0; n < 2; ++n) _Pragma("unroll") for (int k = 0; k < 2; ++k) dst[n][k] = *(const PG8_LAS bf16x8*)(lds + PG8_SB(b, h) + boff + n * 2048 + k * 1024); } while (0)
; #define PG8_MMA(ai, bj, At, Bt) do { __builtin_amdgcn_s_setprio(1); _Pragma("unroll") for (int m = 0; m < 4; ++m) _Pragma("unroll") for (int n = 0; n < 2; ++n) _Pragma("unroll") for (int k = 0; k < 2; ++k) \
;         acc[ai][bj][m][n] = __builtin_amdgcn_mfma_f32_16x16x32_bf16(Bt[n][k], At[m][k], acc[ai][bj][m][n], 0, 0, 0); __builtin_amdgcn_s_setprio(0); } while (0)
; #define PG8_WAIT_V(n) asm volatile("s_waitcnt vmcnt(" #n ")" ::: "memory")
; #define PG8_WAIT_L(n) asm volatile("s_waitcnt lgkmcnt(" #n ")" ::: "memory")
; #define PG8_BAR __builtin_amdgcn_s_barrier()
; #define PG8_SCHED __builtin_amdgcn_sched_barrier(0)
; template <class Epi, class Sched, bool ALIGN_EPI = false, bool SP2 = false>
; __device__ __forceinline__ void gemm_phase(PG8_LAS unsigned char* lds, const Gemm g, const Sched& S, const Epi& E) {
;     ...
;             PG8_WAIT_V(8); PG8_WAIT_L(0); PG8_BAR; PG8_MMA(1, 0, At, B0); PG8_MMA(1, 1, At, B1); PG8_BAR; PG8_SCHED;
;             PG8_LDB(B0, 1, 0); PG8_LDB(B1, 1, 1); PG8_SCHED; PG8_LDA(At, 1, 0); PG8_STAGEA(PG8_SA(0, 1), a2, 1, last);
;             PG8_WAIT_V(8); PG8_WAIT_L(0); PG8_BAR; PG8_MMA(0, 0, At, B0); PG8_MMA(0, 1, At, B1); PG8_BAR; PG8_SCHED;
	s_setprio 1
	v_mfma_f32_16x16x32_bf16 v[58:61], v[148:151], v[180:183], v[58:61]
	v_mfma_f32_16x16x32_bf16 v[62:65], v[156:159], v[180:183], v[62:65]
	v_mfma_f32_16x16x32_bf16 v[42:45], v[148:151], v[188:191], v[42:45]
	v_mfma_f32_16x16x32_bf16 v[46:49], v[156:159], v[188:191], v[46:49]
	v_mfma_f32_16x16x32_bf16 v[26:29], v[148:151], v[196:199], v[26:29]
	v_mfma_f32_16x16x32_bf16 v[30:33], v[156:159], v[196:199], v[30:33]
	v_mfma_f32_16x16x32_bf16 v[10:13], v[148:151], v[208:211], v[10:13]
	v_mfma_f32_16x16x32_bf16 v[14:17], v[156:159], v[208:211], v[14:17]
	v_mfma_f32_16x16x32_bf16 v[58:61], v[152:155], v[184:187], v[58:61]
	v_mfma_f32_16x16x32_bf16 v[62:65], v[160:163], v[184:187], v[62:65]
	v_mfma_f32_16x16x32_bf16 v[42:45], v[152:155], v[192:195], v[42:45]
	v_mfma_f32_16x16x32_bf16 v[46:49], v[160:163], v[192:195], v[46:49]
	v_mfma_f32_16x16x32_bf16 v[26:29], v[152:155], v[204:207], v[26:29]
	v_mfma_f32_16x16x32_bf16 v[30:33], v[160:163], v[204:207], v[30:33]
	v_mfma_f32_16x16x32_bf16 v[10:13], v[152:155], v[212:215], v[10:13]
	v_mfma_f32_16x16x32_bf16 v[14:17], v[160:163], v[212:215], v[14:17]
	v_mfma_f32_16x16x32_bf16 v[50:53], v[164:167], v[180:183], v[50:53]
	v_mfma_f32_16x16x32_bf16 v[54:57], v[172:175], v[180:183], v[54:57]
	v_mfma_f32_16x16x32_bf16 v[34:37], v[164:167], v[188:191], v[34:37]
	v_mfma_f32_16x16x32_bf16 v[38:41], v[172:175], v[188:191], v[38:41]
	v_mfma_f32_16x16x32_bf16 v[18:21], v[164:167], v[196:199], v[18:21]
	v_mfma_f32_16x16x32_bf16 v[22:25], v[172:175], v[196:199], v[22:25]
	v_mfma_f32_16x16x32_bf16 v[6:9], v[164:167], v[208:211], v[6:9]
	v_mfma_f32_16x16x32_bf16 v[2:5], v[172:175], v[208:211], v[2:5]
	v_mfma_f32_16x16x32_bf16 v[50:53], v[168:171], v[184:187], v[50:53]
	v_mfma_f32_16x16x32_bf16 v[54:57], v[176:179], v[184:187], v[54:57]
	v_mfma_f32_16x16x32_bf16 v[34:37], v[168:171], v[192:195], v[34:37]
	v_mfma_f32_16x16x32_bf16 v[38:41], v[176:179], v[192:195], v[38:41]
	v_mfma_f32_16x16x32_bf16 v[18:21], v[168:171], v[204:207], v[18:21]
	v_mfma_f32_16x16x32_bf16 v[22:25], v[176:179], v[204:207], v[22:25]
	v_mfma_f32_16x16x32_bf16 v[6:9], v[168:171], v[212:215], v[6:9]
	v_mfma_f32_16x16x32_bf16 v[2:5], v[176:179], v[212:215], v[2:5]
	s_setprio 0
	s_barrier
	s_add_i32 s84, 0, 0x18000
	v_add_u32_e32 v147, s84, v142
	s_add_i32 s85, 0, 0x1c000
	ds_read_b128 v[148:151], v147
	ds_read_b128 v[152:155], v147 offset:1024
	ds_read_b128 v[156:159], v147 offset:2048
	ds_read_b128 v[160:163], v147 offset:3072
	v_add_u32_e32 v147, s85, v142
	ds_read_b128 v[164:167], v147
	ds_read_b128 v[168:171], v147 offset:1024
	ds_read_b128 v[172:175], v147 offset:2048
	ds_read_b128 v[176:179], v147 offset:3072
	s_add_u32 s62, s62, 0x20000
	s_addc_u32 s63, s63, 0
	s_mov_b32 m0, s67
	v_lshl_add_u64 v[222:223], s[62:63], 0, v[130:131]
	ds_read_b128 v[180:183], v146 offset:32768
	ds_read_b128 v[184:187], v146 offset:33792
	ds_read_b128 v[188:191], v146 offset:34816
	ds_read_b128 v[192:195], v146 offset:35840
	ds_read_b128 v[196:199], v146 offset:36864
	ds_read_b128 v[204:207], v146 offset:37888
	ds_read_b128 v[208:211], v146 offset:38912
	ds_read_b128 v[212:215], v146 offset:39936
	global_load_lds_dwordx4 v[222:223], off
	v_lshl_add_u64 v[222:223], s[62:63], 0, v[134:135]
	s_mov_b32 m0, s68
	s_nop 0
	global_load_lds_dwordx4 v[222:223], off
	s_waitcnt vmcnt(8) lgkmcnt(0)
	s_barrier
	s_setprio 1
	v_mfma_f32_16x16x32_bf16 v[122:125], v[148:151], v[180:183], v[122:125]
	v_mfma_f32_16x16x32_bf16 v[126:129], v[156:159], v[180:183], v[126:129]
	v_mfma_f32_16x16x32_bf16 v[106:109], v[148:151], v[188:191], v[106:109]
	v_mfma_f32_16x16x32_bf16 v[110:113], v[156:159], v[188:191], v[110:113]
	v_mfma_f32_16x16x32_bf16 v[90:93], v[148:151], v[196:199], v[90:93]
	v_mfma_f32_16x16x32_bf16 v[94:97], v[156:159], v[196:199], v[94:97]
	v_mfma_f32_16x16x32_bf16 v[74:77], v[148:151], v[208:211], v[74:77]
	v_mfma_f32_16x16x32_bf16 v[78:81], v[156:159], v[208:211], v[78:81]
	v_mfma_f32_16x16x32_bf16 v[122:125], v[152:155], v[184:187], v[122:125]
	v_mfma_f32_16x16x32_bf16 v[126:129], v[160:163], v[184:187], v[126:129]
	v_mfma_f32_16x16x32_bf16 v[106:109], v[152:155], v[192:195], v[106:109]
	v_mfma_f32_16x16x32_bf16 v[110:113], v[160:163], v[192:195], v[110:113]
	v_mfma_f32_16x16x32_bf16 v[90:93], v[152:155], v[204:207], v[90:93]
	v_mfma_f32_16x16x32_bf16 v[94:97], v[160:163], v[204:207], v[94:97]
	v_mfma_f32_16x16x32_bf16 v[74:77], v[152:155], v[212:215], v[74:77]
	v_mfma_f32_16x16x32_bf16 v[78:81], v[160:163], v[212:215], v[78:81]
	v_mfma_f32_16x16x32_bf16 v[114:117], v[164:167], v[180:183], v[114:117]
	v_mfma_f32_16x16x32_bf16 v[118:121], v[172:175], v[180:183], v[118:121]
	v_mfma_f32_16x16x32_bf16 v[98:101], v[164:167], v[188:191], v[98:101]
	v_mfma_f32_16x16x32_bf16 v[102:105], v[172:175], v[188:191], v[102:105]
	v_mfma_f32_16x16x32_bf16 v[82:85], v[164:167], v[196:199], v[82:85]
	v_mfma_f32_16x16x32_bf16 v[86:89], v[172:175], v[196:199], v[86:89]
	v_mfma_f32_16x16x32_bf16 v[66:69], v[164:167], v[208:211], v[66:69]
	v_mfma_f32_16x16x32_bf16 v[70:73], v[172:175], v[208:211], v[70:73]
	v_mfma_f32_16x16x32_bf16 v[114:117], v[168:171], v[184:187], v[114:117]
	v_mfma_f32_16x16x32_bf16 v[118:121], v[176:179], v[184:187], v[118:121]
	v_mfma_f32_16x16x32_bf16 v[98:101], v[168:171], v[192:195], v[98:101]
	v_mfma_f32_16x16x32_bf16 v[102:105], v[176:179], v[192:195], v[102:105]
	v_mfma_f32_16x16x32_bf16 v[82:85], v[168:171], v[204:207], v[82:85]
	v_mfma_f32_16x16x32_bf16 v[86:89], v[176:179], v[204:207], v[86:89]
	v_mfma_f32_16x16x32_bf16 v[66:69], v[168:171], v[212:215], v[66:69]
	v_mfma_f32_16x16x32_bf16 v[70:73], v[176:179], v[212:215], v[70:73]
	s_setprio 0
	s_barrier
; #define PG8_STAGE(bufoff, gbase, voff) do { _Pragma("unroll") for (int _i = 0; _i < 2; ++_i) \
;         __builtin_amdgcn_global_load_lds((const unsigned*)((const char*)(gbase) + (voff)[_i]), (PG8_LAS unsigned*)(lds + (bufoff) + ldsw + _i * 8192), 16, 0, 0); } while (0)
; #define PG8_LDA(dst, b, h) do { _Pragma("unroll") for (int m = 0; m < 4; ++m) _Pragma("unroll") for (int k = 0; k < 2; ++k) dst[m][k] = *(const PG8_LAS bf16x8*)(lds + PG8_SA(b, h) + aoff + m * 2048 + k * 1024); } while (0)
; #define PG8_MMA(ai, bj, At, Bt) do { __builtin_amdgcn_s_setprio(1); _Pragma("unroll") for (int m = 0; m < 4; ++m) _Pragma("unroll") for (int n = 0; n < 2; ++n) _Pragma("unroll") for (int k = 0; k < 2; ++k) \
;         acc[ai][bj][m][n] = __builtin_amdgcn_mfma_f32_16x16x32_bf16(Bt[n][k], At[m][k], acc[ai][bj][m][n], 0, 0, 0); __builtin_amdgcn_s_setprio(0); } while (0)
; #define PG8_WAIT_V(n) asm volatile("s_waitcnt vmcnt(" #n ")" ::: "memory")
; #define PG8_WAIT_L(n) asm volatile("s_waitcnt lgkmcnt(" #n ")" ::: "memory")
; #define PG8_BAR __builtin_amdgcn_s_barrier()
; #define PG8_SCHED __builtin_amdgcn_sched_barrier(0)
; template <class Epi, class Sched, bool ALIGN_EPI = false, bool SP2 = false>
; __device__ __forceinline__ void gemm_phase(PG8_LAS unsigned char* lds, const Gemm g, const Sched& S, const Epi& E) {
;     ...
;             PG8_LDA(At, 1, 1); PG8_STAGE(PG8_SB(1, 0), b3, voffB); PG8_STAGE(PG8_SB(1, 1), b3 + hstep, voffB); PG8_STAGEA(PG8_SA(1, 0), a3, 0, last);
;             PG8_WAIT_V(8); PG8_WAIT_L(0); PG8_BAR; PG8_MMA(1, 0, At, B0); PG8_MMA(1, 1, At, B1); PG8_BAR; PG8_SCHED;
	s_add_i32 s62, s84, s65
	v_lshl_add_u64 v[200:201], v[200:201], 0, s[18:19]
	s_mov_b32 m0, s62
	ds_read_b128 v[180:183], v146 offset:49152
	ds_read_b128 v[184:187], v146 offset:50176
	ds_read_b128 v[188:191], v146 offset:51200
	ds_read_b128 v[192:195], v146 offset:52224
	ds_read_b128 v[196:199], v146 offset:53248
	ds_read_b128 v[204:207], v146 offset:54272
	ds_read_b128 v[208:211], v146 offset:55296
	ds_read_b128 v[212:215], v146 offset:56320
	global_load_lds_dwordx4 v[200:201], off
	s_add_i32 m0, s62, 0x2000
	s_add_u32 s60, s60, 0x20080
	v_lshl_add_u64 v[200:201], v[216:217], 0, s[18:19]
	s_addc_u32 s61, s61, 0
	s_add_i32 s62, s85, s65
	global_load_lds_dwordx4 v[200:201], off
	v_lshl_add_u64 v[200:201], s[60:61], 0, v[132:133]
	s_mov_b32 m0, s62
	s_nop 0
	global_load_lds_dwordx4 v[200:201], off
	v_lshl_add_u64 v[200:201], s[60:61], 0, v[136:137]
	s_add_i32 m0, s62, 0x2000
	s_nop 0
	global_load_lds_dwordx4 v[200:201], off
	v_lshl_add_u64 v[200:201], v[218:219], 0, s[18:19]
	s_mov_b32 m0, s69
	s_nop 0
	global_load_lds_dwordx4 v[200:201], off
	v_lshl_add_u64 v[200:201], v[220:221], 0, s[18:19]
	s_mov_b32 m0, s74
	s_nop 0
	global_load_lds_dwordx4 v[200:201], off
	s_waitcnt vmcnt(8) lgkmcnt(0)
	s_barrier
	s_setprio 1
	v_mfma_f32_16x16x32_bf16 v[58:61], v[148:151], v[180:183], v[58:61]
	v_mfma_f32_16x16x32_bf16 v[62:65], v[156:159], v[180:183], v[62:65]
	v_mfma_f32_16x16x32_bf16 v[42:45], v[148:151], v[188:191], v[42:45]
	v_mfma_f32_16x16x32_bf16 v[46:49], v[156:159], v[188:191], v[46:49]
	v_mfma_f32_16x16x32_bf16 v[26:29], v[148:151], v[196:199], v[26:29]
	v_mfma_f32_16x16x32_bf16 v[30:33], v[156:159], v[196:199], v[30:33]
	v_mfma_f32_16x16x32_bf16 v[10:13], v[148:151], v[208:211], v[10:13]
	v_mfma_f32_16x16x32_bf16 v[14:17], v[156:159], v[208:211], v[14:17]
	v_mfma_f32_16x16x32_bf16 v[58:61], v[152:155], v[184:187], v[58:61]
	v_mfma_f32_16x16x32_bf16 v[62:65], v[160:163], v[184:187], v[62:65]
	v_mfma_f32_16x16x32_bf16 v[42:45], v[152:155], v[192:195], v[42:45]
	v_mfma_f32_16x16x32_bf16 v[46:49], v[160:163], v[192:195], v[46:49]
	v_mfma_f32_16x16x32_bf16 v[26:29], v[152:155], v[204:207], v[26:29]
	v_mfma_f32_16x16x32_bf16 v[30:33], v[160:163], v[204:207], v[30:33]
	v_mfma_f32_16x16x32_bf16 v[10:13], v[152:155], v[212:215], v[10:13]
	v_mfma_f32_16x16x32_bf16 v[14:17], v[160:163], v[212:215], v[14:17]
	v_mfma_f32_16x16x32_bf16 v[50:53], v[164:167], v[180:183], v[50:53]
	v_mfma_f32_16x16x32_bf16 v[54:57], v[172:175], v[180:183], v[54:57]
	v_mfma_f32_16x16x32_bf16 v[34:37], v[164:167], v[188:191], v[34:37]
	v_mfma_f32_16x16x32_bf16 v[38:41], v[172:175], v[188:191], v[38:41]
	v_mfma_f32_16x16x32_bf16 v[18:21], v[164:167], v[196:199], v[18:21]
	v_mfma_f32_16x16x32_bf16 v[22:25], v[172:175], v[196:199], v[22:25]
	v_mfma_f32_16x16x32_bf16 v[6:9], v[164:167], v[208:211], v[6:9]
	v_mfma_f32_16x16x32_bf16 v[2:5], v[172:175], v[208:211], v[2:5]
	v_mfma_f32_16x16x32_bf16 v[50:53], v[168:171], v[184:187], v[50:53]
	v_mfma_f32_16x16x32_bf16 v[54:57], v[176:179], v[184:187], v[54:57]
	v_mfma_f32_16x16x32_bf16 v[34:37], v[168:171], v[192:195], v[34:37]
	v_mfma_f32_16x16x32_bf16 v[38:41], v[176:179], v[192:195], v[38:41]
	v_mfma_f32_16x16x32_bf16 v[18:21], v[168:171], v[204:207], v[18:21]
	v_mfma_f32_16x16x32_bf16 v[22:25], v[176:179], v[204:207], v[22:25]
	v_mfma_f32_16x16x32_bf16 v[6:9], v[168:171], v[212:215], v[6:9]
	v_mfma_f32_16x16x32_bf16 v[2:5], v[176:179], v[212:215], v[2:5]
	s_setprio 0
	s_barrier
	s_add_i32 s83, s83, 2
	s_add_u32 s58, s58, 0x100
	s_addc_u32 s59, s59, 0
	s_add_u32 s47, s47, 0x100
	s_addc_u32 s49, s49, 0
	s_cmp_gt_u32 s83, 5
	s_cbranch_scc0 .LBB0_927
	s_and_b64 vcc, exec, s[24:25]
	s_cbranch_vccz .LBB0_930
	s_barrier
